# ret_out item loop (both layers): the epilogue's gate-row and ret_g loads are issued at the top of the item's compute body, one drain before the silu math
# speedup vs baseline: 1.0027x; 1.0022x over previous
.LBB0_1275:
	ds_read_b128 v[30:33], v183
	ds_read_b128 v[26:29], v183 offset:64
	ds_read_b128 v[34:37], v184 offset:18432
	ds_read_b128 v[38:41], v184 offset:18496
	s_lshl_b32 s0, s87, 5
	s_sub_i32 s2, s82, s0
	s_lshr_b32 s0, s86, 24
	s_waitcnt lgkmcnt(1)
	v_mfma_f32_16x16x32_bf16 v[34:37], v[34:37], v[30:33], 0
	s_add_i32 s0, s82, s0
	s_ashr_i32 s0, s0, 8
	s_ashr_i32 s1, s0, 31
	s_waitcnt lgkmcnt(0)
	v_mfma_f32_16x16x32_bf16 v[54:57], v[38:41], v[26:29], v[34:37]
	ds_read_b128 v[38:41], v184 offset:20800
	s_ashr_i32 s3, s2, 31
	s_nop 0
	ds_read_b128 v[34:37], v184 offset:20736
	s_lshl_b64 s[0:1], s[0:1], 12
	s_lshl_b64 s[86:87], s[2:3], 7
	s_add_u32 s0, s0, s86
	s_addc_u32 s1, s1, s87
	s_waitcnt lgkmcnt(0)
	v_mfma_f32_16x16x32_bf16 v[34:37], v[34:37], v[30:33], 0
	s_lshl_b32 s82, s97, 7
	v_lshl_add_u64 v[212:213], s[0:1], 0, v[82:83]
	v_mov_b64_e32 v[238:239], s[80:81]
	v_mad_u64_u32 v[238:239], s[98:99], v212, s90, v[238:239]
	v_mad_i32_i24 v239, v213, s90, v239
	v_lshl_add_u64 v[238:239], v[238:239], 0, s[82:83]
	v_lshl_add_u64 v[238:239], v[238:239], 0, v[72:73]
	global_load_dwordx2 v[216:217], v[238:239], off offset:3072
	global_load_dwordx2 v[218:219], v[238:239], off offset:3104
	global_load_dwordx2 v[220:221], v[238:239], off offset:3136
	global_load_dwordx2 v[230:231], v[238:239], off offset:3168
	v_lshl_add_u64 v[238:239], v[84:85], 0, s[82:83]
	v_lshl_add_u64 v[238:239], v[238:239], 0, s[82:83]
	global_load_dwordx4 v[200:203], v[238:239], off
	global_load_dwordx4 v[204:207], v[238:239], off offset:64
	global_load_dwordx4 v[208:211], v[238:239], off offset:128
	global_load_dwordx4 v[212:215], v[238:239], off offset:192
	ds_read_b128 v[58:61], v184 offset:34624
	v_mfma_f32_16x16x32_bf16 v[62:65], v[38:41], v[26:29], v[34:37]
	ds_read_b128 v[38:41], v184 offset:23104
	s_nop 3
	ds_read_b128 v[34:37], v184 offset:23040
	s_waitcnt lgkmcnt(0)
	v_mfma_f32_16x16x32_bf16 v[34:37], v[34:37], v[30:33], 0
	v_mfma_f32_16x16x32_bf16 v[66:69], v[38:41], v[26:29], v[34:37]
	ds_read_b128 v[38:41], v184 offset:25408
	s_nop 5
	ds_read_b128 v[34:37], v184 offset:25344
	s_waitcnt lgkmcnt(0)
	v_mfma_f32_16x16x32_bf16 v[34:37], v[34:37], v[30:33], 0
	v_mfma_f32_16x16x32_bf16 v[50:53], v[38:41], v[26:29], v[34:37]
	ds_read_b128 v[38:41], v184 offset:27712
	s_nop 5
	ds_read_b128 v[34:37], v184 offset:27648
	s_waitcnt lgkmcnt(0)
	v_mfma_f32_16x16x32_bf16 v[34:37], v[34:37], v[30:33], 0
	v_mfma_f32_16x16x32_bf16 v[46:49], v[38:41], v[26:29], v[34:37]
	ds_read_b128 v[38:41], v184 offset:30016
	s_nop 5
	ds_read_b128 v[34:37], v184 offset:29952
	s_waitcnt lgkmcnt(0)
	v_mfma_f32_16x16x32_bf16 v[34:37], v[34:37], v[30:33], 0
	v_mfma_f32_16x16x32_bf16 v[42:45], v[38:41], v[26:29], v[34:37]
	ds_read_b128 v[38:41], v184 offset:32320
	s_nop 5
	ds_read_b128 v[34:37], v184 offset:32256
	s_waitcnt lgkmcnt(0)
	v_mfma_f32_16x16x32_bf16 v[34:37], v[34:37], v[30:33], 0
	v_mfma_f32_16x16x32_bf16 v[38:41], v[38:41], v[26:29], v[34:37]
	s_nop 6
	ds_read_b128 v[34:37], v184 offset:34560
	s_waitcnt lgkmcnt(0)
	v_mfma_f32_16x16x32_bf16 v[34:37], v[34:37], v[30:33], 0
	v_mfma_f32_16x16x32_bf16 v[34:37], v[58:61], v[26:29], v[34:37]
	v_mul_f32_e32 v58, v107, v89
	v_mul_f32_e32 v59, v108, v87
	v_cndmask_b32_e64 v58, v59, v58, s[8:9]
	v_mul_f32_e32 v59, v107, v91
	v_mul_f32_e32 v60, v108, v93
	v_cndmask_b32_e64 v59, v59, v60, s[10:11]
	v_mul_f32_e32 v58, 0x3fb8aa3b, v58
	v_mul_f32_e32 v59, 0x3fb8aa3b, v59
	v_exp_f32_e32 v58, v58
	v_exp_f32_e32 v59, v59
	v_mul_f32_e32 v60, v108, v120
	v_pk_mul_f32 v[58:59], v[58:59], v[54:55]
	v_mul_f32_e32 v54, v107, v119
	v_mul_f32_e32 v55, v108, v118
	v_cndmask_b32_e64 v54, v55, v54, s[12:13]
	v_mul_f32_e32 v55, v107, v121
	v_cndmask_b32_e64 v55, v60, v55, s[14:15]
	v_mul_f32_e32 v54, 0x3fb8aa3b, v54
	v_mul_f32_e32 v55, 0x3fb8aa3b, v55
	v_exp_f32_e32 v54, v54
	v_exp_f32_e32 v55, v55
	v_cvt_pk_bf16_f32 v58, v58, v59
	v_pk_mul_f32 v[60:61], v[54:55], v[56:57]
	v_mul_f32_e32 v54, v107, v123
	v_mul_f32_e32 v55, v108, v122
	v_cndmask_b32_e64 v54, v55, v54, s[16:17]
	v_mul_f32_e32 v55, v107, v125
	v_mul_f32_e32 v56, v108, v124
	v_cndmask_b32_e64 v55, v56, v55, s[18:19]
	v_mul_f32_e32 v54, 0x3fb8aa3b, v54
	v_mul_f32_e32 v55, 0x3fb8aa3b, v55
	v_exp_f32_e32 v54, v54
	v_exp_f32_e32 v55, v55
	v_mul_f32_e32 v56, v108, v128
	v_mul_f32_e32 v57, v108, v134
	v_cvt_pk_bf16_f32 v59, v60, v61
	v_pk_mul_f32 v[62:63], v[54:55], v[62:63]
	v_mul_f32_e32 v54, v107, v127
	v_mul_f32_e32 v55, v108, v126
	v_cndmask_b32_e64 v54, v55, v54, s[20:21]
	v_mul_f32_e32 v55, v107, v129
	v_cndmask_b32_e64 v55, v56, v55, s[22:23]
	v_mul_f32_e32 v54, 0x3fb8aa3b, v54
	v_mul_f32_e32 v55, 0x3fb8aa3b, v55
	v_exp_f32_e32 v54, v54
	v_exp_f32_e32 v55, v55
	v_mul_f32_e32 v56, v108, v132
	v_cvt_pk_bf16_f32 v60, v62, v63
	v_pk_mul_f32 v[64:65], v[54:55], v[64:65]
	v_mul_f32_e32 v54, v107, v131
	v_mul_f32_e32 v55, v108, v130
	v_cndmask_b32_e64 v54, v55, v54, s[24:25]
	v_mul_f32_e32 v55, v107, v133
	v_cndmask_b32_e64 v55, v56, v55, s[26:27]
	v_mul_f32_e32 v54, 0x3fb8aa3b, v54
	v_mul_f32_e32 v55, 0x3fb8aa3b, v55
	v_exp_f32_e32 v54, v54
	v_exp_f32_e32 v55, v55
	v_mul_f32_e32 v56, v107, v135
	v_cndmask_b32_e64 v56, v57, v56, s[28:29]
	v_mul_f32_e32 v57, v107, v137
	v_pk_mul_f32 v[54:55], v[54:55], v[66:67]
	v_mul_f32_e32 v66, v108, v136
	v_cndmask_b32_e64 v57, v66, v57, s[30:31]
	v_mul_f32_e32 v56, 0x3fb8aa3b, v56
	v_mul_f32_e32 v57, 0x3fb8aa3b, v57
	v_exp_f32_e32 v56, v56
	v_exp_f32_e32 v57, v57
	v_mul_f32_e32 v66, v107, v139
	v_mul_f32_e32 v67, v108, v138
	v_cndmask_b32_e64 v66, v67, v66, s[34:35]
	v_pk_mul_f32 v[56:57], v[56:57], v[68:69]
	v_mul_f32_e32 v67, v107, v141
	v_mul_f32_e32 v68, v108, v140
	v_cndmask_b32_e64 v67, v68, v67, s[36:37]
	v_mul_f32_e32 v66, 0x3fb8aa3b, v66
	v_mul_f32_e32 v67, 0x3fb8aa3b, v67
	v_exp_f32_e32 v66, v66
	v_exp_f32_e32 v67, v67
	v_mul_f32_e32 v68, v108, v144
	v_cvt_pk_bf16_f32 v61, v64, v65
	v_cvt_pk_bf16_f32 v54, v54, v55
	v_pk_mul_f32 v[50:51], v[66:67], v[50:51]
	v_mul_f32_e32 v66, v107, v143
	v_mul_f32_e32 v67, v108, v142
	v_cndmask_b32_e64 v66, v67, v66, s[38:39]
	v_mul_f32_e32 v67, v107, v145
	v_cndmask_b32_e64 v67, v68, v67, s[40:41]
	v_mul_f32_e32 v66, 0x3fb8aa3b, v66
	v_mul_f32_e32 v67, 0x3fb8aa3b, v67
	v_exp_f32_e32 v66, v66
	v_exp_f32_e32 v67, v67
	v_mul_f32_e32 v68, v108, v148
	v_cvt_pk_bf16_f32 v55, v56, v57
	v_cvt_pk_bf16_f32 v56, v50, v51
	v_pk_mul_f32 v[52:53], v[66:67], v[52:53]
	v_mul_f32_e32 v66, v107, v147
	v_mul_f32_e32 v67, v108, v146
	v_cndmask_b32_e64 v66, v67, v66, s[42:43]
	v_mul_f32_e32 v67, v107, v149
	v_cndmask_b32_e64 v67, v68, v67, s[44:45]
	v_mul_f32_e32 v66, 0x3fb8aa3b, v66
	v_mul_f32_e32 v67, 0x3fb8aa3b, v67
	v_exp_f32_e32 v66, v66
	v_exp_f32_e32 v67, v67
	v_mul_f32_e32 v68, v108, v152
	v_cvt_pk_bf16_f32 v57, v52, v53
	v_pk_mul_f32 v[46:47], v[66:67], v[46:47]
	v_mul_f32_e32 v66, v107, v151
	v_mul_f32_e32 v67, v108, v150
	v_cndmask_b32_e64 v66, v67, v66, s[46:47]
	v_mul_f32_e32 v67, v107, v153
	v_cndmask_b32_e64 v67, v68, v67, s[48:49]
	v_mul_f32_e32 v66, 0x3fb8aa3b, v66
	v_mul_f32_e32 v67, 0x3fb8aa3b, v67
	v_exp_f32_e32 v66, v66
	v_exp_f32_e32 v67, v67
	v_mul_f32_e32 v68, v108, v156
	v_cvt_pk_bf16_f32 v46, v46, v47
	v_pk_mul_f32 v[48:49], v[66:67], v[48:49]
	v_mul_f32_e32 v66, v107, v155
	v_mul_f32_e32 v67, v108, v154
	v_cndmask_b32_e64 v66, v67, v66, s[50:51]
	v_mul_f32_e32 v67, v107, v157
	v_cndmask_b32_e64 v67, v68, v67, s[52:53]
	v_mul_f32_e32 v66, 0x3fb8aa3b, v66
	v_mul_f32_e32 v67, 0x3fb8aa3b, v67
	v_exp_f32_e32 v66, v66
	v_exp_f32_e32 v67, v67
	v_mul_f32_e32 v68, v108, v160
	v_cvt_pk_bf16_f32 v47, v48, v49
	v_pk_mul_f32 v[42:43], v[66:67], v[42:43]
	v_mul_f32_e32 v66, v107, v159
	v_mul_f32_e32 v67, v108, v158
	v_cndmask_b32_e64 v66, v67, v66, s[54:55]
	v_mul_f32_e32 v67, v107, v161
	v_cndmask_b32_e64 v67, v68, v67, s[94:95]
	v_mul_f32_e32 v66, 0x3fb8aa3b, v66
	v_mul_f32_e32 v67, 0x3fb8aa3b, v67
	v_exp_f32_e32 v66, v66
	v_exp_f32_e32 v67, v67
	v_mul_f32_e32 v68, v108, v164
	v_cvt_pk_bf16_f32 v48, v42, v43
	v_pk_mul_f32 v[44:45], v[66:67], v[44:45]
	v_mul_f32_e32 v66, v107, v163
	v_mul_f32_e32 v67, v108, v162
	v_cndmask_b32_e64 v66, v67, v66, s[58:59]
	v_mul_f32_e32 v67, v107, v165
	v_cndmask_b32_e64 v67, v68, v67, s[60:61]
	v_mul_f32_e32 v66, 0x3fb8aa3b, v66
	v_mul_f32_e32 v67, 0x3fb8aa3b, v67
	v_exp_f32_e32 v66, v66
	v_exp_f32_e32 v67, v67
	v_mul_f32_e32 v68, v108, v168
	v_cvt_pk_bf16_f32 v49, v44, v45
	v_pk_mul_f32 v[38:39], v[66:67], v[38:39]
	v_mul_f32_e32 v66, v107, v167
	v_mul_f32_e32 v67, v108, v166
	v_cndmask_b32_e64 v66, v67, v66, s[62:63]
	v_mul_f32_e32 v67, v107, v169
	v_cndmask_b32_e64 v67, v68, v67, s[64:65]
	v_mul_f32_e32 v66, 0x3fb8aa3b, v66
	v_mul_f32_e32 v67, 0x3fb8aa3b, v67
	v_exp_f32_e32 v66, v66
	v_exp_f32_e32 v67, v67
	v_mul_f32_e32 v68, v108, v172
	v_cvt_pk_bf16_f32 v38, v38, v39
	v_pk_mul_f32 v[40:41], v[66:67], v[40:41]
	v_mul_f32_e32 v66, v107, v171
	v_mul_f32_e32 v67, v108, v170
	v_cndmask_b32_e64 v66, v67, v66, s[66:67]
	v_mul_f32_e32 v67, v107, v173
	v_cndmask_b32_e64 v67, v68, v67, s[68:69]
	v_mul_f32_e32 v66, 0x3fb8aa3b, v66
	v_mul_f32_e32 v67, 0x3fb8aa3b, v67
	v_exp_f32_e32 v66, v66
	v_exp_f32_e32 v67, v67
	v_mul_f32_e32 v68, v108, v176
	v_cvt_pk_bf16_f32 v39, v40, v41
	v_pk_mul_f32 v[34:35], v[66:67], v[34:35]
	v_mul_f32_e32 v66, v107, v175
	v_mul_f32_e32 v67, v108, v174
	v_cndmask_b32_e64 v66, v67, v66, s[70:71]
	v_mul_f32_e32 v67, v107, v177
	v_cndmask_b32_e64 v67, v68, v67, s[72:73]
	v_mul_f32_e32 v66, 0x3fb8aa3b, v66
	v_mul_f32_e32 v67, 0x3fb8aa3b, v67
	v_exp_f32_e32 v66, v66
	v_exp_f32_e32 v67, v67
	v_cvt_pk_bf16_f32 v40, v34, v35
	v_pk_mul_f32 v[36:37], v[66:67], v[36:37]
	ds_read_b64_tr_b16 v[64:65], v185 offset:39168
	ds_read_b64_tr_b16 v[62:63], v185 offset:36864
	ds_read_b64_tr_b16 v[66:67], v185 offset:36896
	ds_read_b64_tr_b16 v[68:69], v185 offset:39200
	ds_read_b64_tr_b16 v[110:111], v185 offset:36928
	ds_read_b64_tr_b16 v[112:113], v185 offset:39232
	ds_read_b64_tr_b16 v[192:193], v185 offset:36960
	ds_read_b64_tr_b16 v[194:195], v185 offset:39264
	s_waitcnt lgkmcnt(6)
	v_mfma_f32_16x16x32_bf16 v[62:65], v[62:65], v[58:61], 0
	v_cvt_pk_bf16_f32 v41, v36, v37
	s_waitcnt lgkmcnt(4)
	v_mfma_f32_16x16x32_bf16 v[66:69], v[66:69], v[58:61], 0
	s_waitcnt lgkmcnt(2)
	v_mfma_f32_16x16x32_bf16 v[110:113], v[110:113], v[58:61], 0
	s_waitcnt lgkmcnt(0)
	v_mfma_f32_16x16x32_bf16 v[58:61], v[192:195], v[58:61], 0
	ds_read_b64_tr_b16 v[52:53], v186 offset:39168
	ds_read_b64_tr_b16 v[50:51], v186 offset:36864
	ds_read_b64_tr_b16 v[192:193], v186 offset:36896
	ds_read_b64_tr_b16 v[194:195], v186 offset:39200
	s_waitcnt lgkmcnt(2)
	v_mfma_f32_16x16x32_bf16 v[50:53], v[50:53], v[54:57], v[62:65]
	s_waitcnt lgkmcnt(0)
	v_mfma_f32_16x16x32_bf16 v[62:65], v[192:195], v[54:57], v[66:69]
	s_nop 2
	ds_read_b64_tr_b16 v[66:67], v186 offset:36928
	ds_read_b64_tr_b16 v[68:69], v186 offset:39232
	s_waitcnt lgkmcnt(0)
	v_mfma_f32_16x16x32_bf16 v[66:69], v[66:69], v[54:57], v[110:113]
	s_nop 2
	ds_read_b64_tr_b16 v[110:111], v186 offset:36960
	ds_read_b64_tr_b16 v[112:113], v186 offset:39264
	s_waitcnt lgkmcnt(0)
	v_mfma_f32_16x16x32_bf16 v[54:57], v[110:113], v[54:57], v[58:61]
	ds_read_b64_tr_b16 v[44:45], v187 offset:39168
	ds_read_b64_tr_b16 v[42:43], v187 offset:36864
	s_nop 0
	ds_read_b64_tr_b16 v[58:59], v187 offset:36896
	ds_read_b64_tr_b16 v[60:61], v187 offset:39200
	s_waitcnt lgkmcnt(2)
	v_mfma_f32_16x16x32_bf16 v[42:45], v[42:45], v[46:49], v[50:53]
	s_nop 2
	ds_read_b64_tr_b16 v[50:51], v187 offset:36928
	ds_read_b64_tr_b16 v[52:53], v187 offset:39232
	s_waitcnt lgkmcnt(2)
	v_mfma_f32_16x16x32_bf16 v[58:61], v[58:61], v[46:49], v[62:65]
	s_waitcnt lgkmcnt(0)
	v_mfma_f32_16x16x32_bf16 v[62:65], v[50:53], v[46:49], v[66:69]
	ds_read_b64_tr_b16 v[50:51], v187 offset:36960
	ds_read_b64_tr_b16 v[52:53], v187 offset:39264
	s_waitcnt lgkmcnt(0)
	v_mfma_f32_16x16x32_bf16 v[54:57], v[50:53], v[46:49], v[54:57]
	ds_read_b64_tr_b16 v[36:37], v188 offset:39168
	ds_read_b64_tr_b16 v[34:35], v188 offset:36864
	ds_read_b64_tr_b16 v[46:47], v188 offset:36896
	ds_read_b64_tr_b16 v[48:49], v188 offset:39200
	s_waitcnt lgkmcnt(2)
	v_mfma_f32_16x16x32_bf16 v[50:53], v[34:37], v[38:41], v[42:45]
	s_nop 2
	ds_read_b64_tr_b16 v[42:43], v188 offset:36928
	ds_read_b64_tr_b16 v[44:45], v188 offset:39232
	s_waitcnt lgkmcnt(2)
	v_mfma_f32_16x16x32_bf16 v[34:37], v[46:49], v[38:41], v[58:61]
	s_waitcnt lgkmcnt(0)
	v_mfma_f32_16x16x32_bf16 v[46:49], v[42:45], v[38:41], v[62:65]
	ds_read_b64_tr_b16 v[42:43], v188 offset:36960
	ds_read_b64_tr_b16 v[44:45], v188 offset:39264
	ds_read_b128 v[110:113], v178 offset:59968
	ds_read_b128 v[62:65], v178 offset:57664
	s_waitcnt lgkmcnt(2)
	v_mfma_f32_16x16x32_bf16 v[192:195], v[42:45], v[38:41], v[54:57]
	ds_read_b128 v[38:41], v178 offset:55296
	s_nop 1
	ds_read_b128 v[54:57], v178 offset:55360
	ds_read_b128 v[42:45], v178 offset:64512
	s_waitcnt lgkmcnt(2)
	v_mfma_f32_16x16x32_bf16 v[38:41], v[38:41], v[30:33], 0
	ds_read_b128 v[66:69], v180 offset:64512
	ds_read_b128 v[196:199], v181 offset:64512
	s_waitcnt lgkmcnt(3)
	v_mfma_f32_16x16x32_bf16 v[54:57], v[54:57], v[26:29], v[38:41]
	s_nop 3
	ds_read_b128 v[38:41], v178 offset:64576
	s_waitcnt lgkmcnt(3)
	v_mfma_f32_16x16x32_bf16 v[42:45], v[42:45], v[30:33], 0
	s_waitcnt lgkmcnt(0)
	v_mfma_f32_16x16x32_bf16 v[58:61], v[38:41], v[26:29], v[42:45]
	ds_read_b128 v[38:41], v178 offset:57600
	s_nop 4
	ds_read_b128 v[42:45], v179 offset:64512
	s_waitcnt lgkmcnt(1)
	v_mfma_f32_16x16x32_bf16 v[38:41], v[38:41], v[30:33], 0
	v_mfma_f32_16x16x32_bf16 v[38:41], v[62:65], v[26:29], v[38:41]
	ds_read_b128 v[62:65], v179 offset:64576
	s_waitcnt lgkmcnt(1)
	v_mfma_f32_16x16x32_bf16 v[42:45], v[42:45], v[30:33], 0
	s_waitcnt lgkmcnt(0)
	v_mfma_f32_16x16x32_bf16 v[42:45], v[62:65], v[26:29], v[42:45]
	ds_read_b128 v[62:65], v178 offset:59904
	s_waitcnt lgkmcnt(0)
	v_mfma_f32_16x16x32_bf16 v[62:65], v[62:65], v[30:33], 0
	v_mfma_f32_16x16x32_bf16 v[62:65], v[110:113], v[26:29], v[62:65]
	ds_read_b128 v[110:113], v180 offset:64576
	v_mfma_f32_16x16x32_bf16 v[66:69], v[66:69], v[30:33], 0
	s_waitcnt lgkmcnt(0)
	v_mfma_f32_16x16x32_bf16 v[66:69], v[110:113], v[26:29], v[66:69]
	ds_read_b128 v[110:113], v178 offset:62208
	s_waitcnt lgkmcnt(0)
	v_mfma_f32_16x16x32_bf16 v[110:113], v[110:113], v[30:33], 0
	v_mfma_f32_16x16x32_bf16 v[30:33], v[196:199], v[30:33], 0
	ds_read_b128 v[196:199], v178 offset:62272
	s_waitcnt lgkmcnt(0)
	v_mfma_f32_16x16x32_bf16 v[196:199], v[196:199], v[26:29], v[110:113]
	s_nop 3
	ds_read_b128 v[110:113], v181 offset:64576
	s_waitcnt lgkmcnt(0)
	v_mfma_f32_16x16x32_bf16 v[26:29], v[110:113], v[26:29], v[30:33]
	s_nop 2
	v_mul_f32_e32 v30, v108, v1
	v_mul_f32_e32 v30, 0x3fb8aa3b, v30
	v_exp_f32_e32 v110, v30
	v_mul_f32_e32 v30, v107, v71
	v_mul_f32_e32 v30, 0x3fb8aa3b, v30
	v_exp_f32_e32 v112, v30
	s_nop 0
	v_pk_mul_f32 v[26:27], v[112:113], v[26:27] op_sel_hi:[0,1]
	v_pk_fma_f32 v[26:27], v[110:111], v[196:197], v[26:27] op_sel_hi:[0,1,1]
	v_pk_add_f32 v[32:33], v[192:193], v[26:27]
	v_pk_mul_f32 v[26:27], v[112:113], v[28:29] op_sel_hi:[0,1]
	v_pk_fma_f32 v[26:27], v[110:111], v[198:199], v[26:27] op_sel_hi:[0,1,1]
	v_pk_add_f32 v[108:109], v[194:195], v[26:27]
	v_lshl_add_u64 v[26:27], s[0:1], 0, v[82:83]
	v_mov_b64_e32 v[28:29], s[80:81]
	v_mad_u64_u32 v[28:29], s[0:1], v26, s90, v[28:29]
	v_pk_mul_f32 v[30:31], v[112:113], v[66:67] op_sel_hi:[0,1]
	v_mad_i32_i24 v29, v27, s90, v29
	v_lshlrev_b64 v[26:27], 12, v[26:27]
	v_pk_fma_f32 v[30:31], v[110:111], v[62:63], v[30:31] op_sel_hi:[0,1,1]
	v_lshl_add_u64 v[28:29], v[28:29], 0, s[82:83]
	v_lshl_add_u64 v[26:27], s[92:93], 0, v[26:27]
	v_pk_add_f32 v[66:67], v[46:47], v[30:31]
	v_lshl_add_u64 v[46:47], v[28:29], 0, v[72:73]
	v_lshl_add_u64 v[26:27], v[26:27], 0, s[82:83]
	s_lshl_b32 s82, s97, 8
	v_lshl_add_u64 v[30:31], v[26:27], 0, v[72:73]
	v_lshl_add_u64 v[62:63], v[84:85], 0, s[82:83]
	s_waitcnt vmcnt(0)
	v_mov_b64 v[114:115], v[216:217]
	s_nop 1
	v_mov_b64 v[26:27], v[200:201]
	v_mov_b64 v[28:29], v[202:203]
	v_pk_mul_f32 v[60:61], v[112:113], v[60:61] op_sel_hi:[0,1]
	v_pk_fma_f32 v[56:57], v[110:111], v[56:57], v[60:61] op_sel_hi:[0,1,1]
	v_pk_add_f32 v[52:53], v[52:53], v[56:57]
	v_pk_mul_f32 v[56:57], v[112:113], v[58:59] op_sel_hi:[0,1]
	v_pk_fma_f32 v[54:55], v[110:111], v[54:55], v[56:57] op_sel_hi:[0,1,1]
	v_pk_add_f32 v[54:55], v[50:51], v[54:55]
	v_pk_mul_f32 v[44:45], v[112:113], v[44:45] op_sel_hi:[0,1]
	v_add_f32_e32 v50, 0, v54
	v_add_f32_e32 v56, v55, v50
	v_add_f32_e32 v56, v52, v56
	s_mov_b32 s82, s96
	v_lshlrev_b32_e32 v57, 16, v114
	v_mul_f32_e32 v50, 0xbfb8aa3b, v57
	v_fma_f32 v51, v57, s91, -v50
	v_rndne_f32_e32 v59, v50
	v_fmac_f32_e32 v51, 0xb2a5705f, v57
	v_sub_f32_e32 v50, v50, v59
	v_add_f32_e32 v50, v50, v51
	v_exp_f32_e32 v50, v50
	v_cvt_i32_f32_e32 v51, v59
	v_and_b32_e32 v58, 0xffff0000, v114
	v_cmp_nlt_f32_e32 vcc, s89, v57
	v_lshlrev_b32_e32 v60, 16, v115
	v_ldexp_f32 v50, v50, v51
	v_mul_f32_e32 v51, 0xbfb8aa3b, v58
	v_fma_f32 v59, v58, s91, -v51
	v_rndne_f32_e32 v103, v51
	v_fmac_f32_e32 v59, 0xb2a5705f, v58
	v_sub_f32_e32 v51, v51, v103
	v_add_f32_e32 v51, v51, v59
	v_exp_f32_e32 v51, v51
	v_cvt_i32_f32_e32 v59, v103
	v_cndmask_b32_e32 v50, 0, v50, vcc
	v_cmp_ngt_f32_e32 vcc, s88, v57
	v_and_b32_e32 v61, 0xffff0000, v115
	v_ldexp_f32 v51, v51, v59
	v_cndmask_b32_e32 v50, v191, v50, vcc
	v_cmp_nlt_f32_e32 vcc, s89, v58
	s_nop 1
	v_cndmask_b32_e32 v51, 0, v51, vcc
	v_cmp_ngt_f32_e32 vcc, s88, v58
	s_nop 1
	v_cndmask_b32_e32 v51, v191, v51, vcc
	v_pk_add_f32 v[50:51], v[50:51], 1.0 op_sel_hi:[1,0]
	s_nop 0
	v_div_scale_f32 v59, s[0:1], v51, v51, v58
	v_rcp_f32_e32 v103, v59
	s_nop 0
	v_fma_f32 v105, -v59, v103, 1.0
	v_fmac_f32_e32 v103, v105, v103
	v_div_scale_f32 v105, vcc, v58, v51, v58
	v_mul_f32_e32 v107, v105, v103
	v_fma_f32 v111, -v59, v107, v105
	v_fmac_f32_e32 v107, v111, v103
	v_fma_f32 v59, -v59, v107, v105
	v_div_fmas_f32 v59, v59, v103, v107
	v_div_fixup_f32 v51, v59, v51, v58
	v_div_scale_f32 v58, s[0:1], v50, v50, v57
	v_rcp_f32_e32 v59, v58
	v_pk_fma_f32 v[40:41], v[110:111], v[40:41], v[44:45] op_sel_hi:[0,1,1]
	v_pk_add_f32 v[36:37], v[36:37], v[40:41]
	v_pk_mul_f32 v[40:41], v[112:113], v[42:43] op_sel_hi:[0,1]
	v_fma_f32 v103, -v58, v59, 1.0
	v_fmac_f32_e32 v59, v103, v59
	v_div_scale_f32 v103, vcc, v57, v50, v57
	v_mul_f32_e32 v105, v103, v59
	v_fma_f32 v107, -v58, v105, v103
	v_fmac_f32_e32 v105, v107, v59
	v_fma_f32 v58, -v58, v105, v103
	v_div_fmas_f32 v58, v58, v59, v105
	v_div_fixup_f32 v50, v58, v50, v57
	v_add_f32_e32 v58, v53, v56
	v_pk_mul_f32 v[56:57], v[112:113], v[68:69] op_sel_hi:[0,1]
	v_pk_fma_f32 v[56:57], v[110:111], v[64:65], v[56:57] op_sel_hi:[0,1,1]
	v_pk_add_f32 v[56:57], v[48:49], v[56:57]
	v_mul_f32_e32 v48, 0xbfb8aa3b, v60
	v_fma_f32 v49, v60, s91, -v48
	v_rndne_f32_e32 v59, v48
	v_fmac_f32_e32 v49, 0xb2a5705f, v60
	v_sub_f32_e32 v48, v48, v59
	v_add_f32_e32 v48, v48, v49
	v_exp_f32_e32 v48, v48
	v_cvt_i32_f32_e32 v49, v59
	v_cmp_nlt_f32_e32 vcc, s89, v60
	v_pk_fma_f32 v[38:39], v[110:111], v[38:39], v[40:41] op_sel_hi:[0,1,1]
	v_pk_add_f32 v[34:35], v[34:35], v[38:39]
	v_ldexp_f32 v48, v48, v49
	v_mul_f32_e32 v49, 0xbfb8aa3b, v61
	v_fma_f32 v59, v61, s91, -v49
	v_rndne_f32_e32 v64, v49
	v_fmac_f32_e32 v59, 0xb2a5705f, v61
	v_sub_f32_e32 v49, v49, v64
	v_add_f32_e32 v49, v49, v59
	v_exp_f32_e32 v49, v49
	v_cvt_i32_f32_e32 v59, v64
	v_cndmask_b32_e32 v48, 0, v48, vcc
	v_cmp_ngt_f32_e32 vcc, s88, v60
	v_add_f32_e32 v38, v58, v34
	v_ldexp_f32 v49, v49, v59
	v_cndmask_b32_e32 v48, v191, v48, vcc
	v_cmp_nlt_f32_e32 vcc, s89, v61
	v_add_f32_e32 v42, v35, v38
	s_nop 0
	v_cndmask_b32_e32 v49, 0, v49, vcc
	v_cmp_ngt_f32_e32 vcc, s88, v61
	s_nop 1
	v_cndmask_b32_e32 v49, v191, v49, vcc
	v_pk_add_f32 v[48:49], v[48:49], 1.0 op_sel_hi:[1,0]
	s_nop 0
	v_div_scale_f32 v59, s[0:1], v49, v49, v61
	v_rcp_f32_e32 v64, v59
	s_nop 0
	v_fma_f32 v65, -v59, v64, 1.0
	v_fmac_f32_e32 v64, v65, v64
	v_div_scale_f32 v65, vcc, v61, v49, v61
	v_mul_f32_e32 v68, v65, v64
	v_fma_f32 v69, -v59, v68, v65
	v_fmac_f32_e32 v68, v69, v64
	v_fma_f32 v59, -v59, v68, v65
	v_div_fmas_f32 v59, v59, v64, v68
	v_div_fixup_f32 v49, v59, v49, v61
	v_div_scale_f32 v59, s[0:1], v48, v48, v60
	v_rcp_f32_e32 v61, v59
	s_nop 0
	v_fma_f32 v64, -v59, v61, 1.0
	v_fmac_f32_e32 v61, v64, v61
	v_div_scale_f32 v64, vcc, v60, v48, v60
	v_mul_f32_e32 v65, v64, v61
	v_fma_f32 v68, -v59, v65, v64
	v_fmac_f32_e32 v65, v68, v61
	v_fma_f32 v59, -v59, v65, v64
	v_div_fmas_f32 v59, v59, v61, v65
	v_div_fixup_f32 v48, v59, v48, v60
	v_mov_b64 v[60:61], v[218:219]
	v_lshlrev_b32_e32 v40, 16, v60
	v_mul_f32_e32 v38, 0xbfb8aa3b, v40
	v_fma_f32 v39, v40, s91, -v38
	v_rndne_f32_e32 v43, v38
	v_fmac_f32_e32 v39, 0xb2a5705f, v40
	v_sub_f32_e32 v38, v38, v43
	v_add_f32_e32 v38, v38, v39
	v_exp_f32_e32 v38, v38
	v_cvt_i32_f32_e32 v39, v43
	v_and_b32_e32 v41, 0xffff0000, v60
	v_cmp_nlt_f32_e32 vcc, s89, v40
	v_lshlrev_b32_e32 v65, 16, v61
	v_ldexp_f32 v38, v38, v39
	v_mul_f32_e32 v39, 0xbfb8aa3b, v41
	v_fma_f32 v43, v41, s91, -v39
	v_rndne_f32_e32 v44, v39
	v_fmac_f32_e32 v43, 0xb2a5705f, v41
	v_sub_f32_e32 v39, v39, v44
	v_add_f32_e32 v39, v39, v43
	v_exp_f32_e32 v39, v39
	v_cvt_i32_f32_e32 v43, v44
	v_cndmask_b32_e32 v38, 0, v38, vcc
	v_cmp_ngt_f32_e32 vcc, s88, v40
	v_and_b32_e32 v103, 0xffff0000, v61
	v_ldexp_f32 v39, v39, v43
	v_cndmask_b32_e32 v38, v191, v38, vcc
	v_cmp_nlt_f32_e32 vcc, s89, v41
	s_nop 1
	v_cndmask_b32_e32 v39, 0, v39, vcc
	v_cmp_ngt_f32_e32 vcc, s88, v41
	s_nop 1
	v_cndmask_b32_e32 v39, v191, v39, vcc
	v_pk_add_f32 v[38:39], v[38:39], 1.0 op_sel_hi:[1,0]
	s_nop 0
	v_div_scale_f32 v43, s[0:1], v39, v39, v41
	v_rcp_f32_e32 v44, v43
	s_nop 0
	v_fma_f32 v45, -v43, v44, 1.0
	v_fmac_f32_e32 v44, v45, v44
	v_div_scale_f32 v45, vcc, v41, v39, v41
	v_mul_f32_e32 v58, v45, v44
	v_fma_f32 v59, -v43, v58, v45
	v_fmac_f32_e32 v58, v59, v44
	v_fma_f32 v43, -v43, v58, v45
	v_div_fmas_f32 v43, v43, v44, v58
	v_div_fixup_f32 v41, v43, v39, v41
	v_div_scale_f32 v39, s[0:1], v38, v38, v40
	v_rcp_f32_e32 v43, v39
	s_nop 0
	v_fma_f32 v44, -v39, v43, 1.0
	v_fmac_f32_e32 v43, v44, v43
	v_div_scale_f32 v44, vcc, v40, v38, v40
	v_mul_f32_e32 v45, v44, v43
	v_fma_f32 v58, -v39, v45, v44
	v_fmac_f32_e32 v45, v58, v43
	v_fma_f32 v39, -v39, v45, v44
	v_div_fmas_f32 v39, v39, v43, v45
	v_div_fixup_f32 v40, v39, v38, v40
	v_add_f32_e32 v38, v36, v42
	v_add_f32_e32 v38, v37, v38
	v_add_f32_e32 v38, v38, v66
	v_add_f32_e32 v38, v67, v38
	v_add_f32_e32 v38, v56, v38
	v_add_f32_e32 v38, v57, v38
	v_add_f32_e32 v38, v38, v32
	v_add_f32_e32 v38, v33, v38
	v_add_f32_e32 v38, v108, v38
	v_add_f32_e32 v38, v109, v38
	ds_bpermute_b32 v39, v116, v38
	v_cmp_nlt_f32_e32 vcc, s89, v65
	s_waitcnt lgkmcnt(0)
	v_add_f32_e32 v38, v38, v39
	ds_bpermute_b32 v39, v117, v38
	s_waitcnt lgkmcnt(0)
	v_add_f32_e32 v38, v38, v39
	v_mul_f32_e32 v64, 0x3c800000, v38
	v_pk_add_f32 v[38:39], v[56:57], v[64:65] op_sel_hi:[1,0] neg_lo:[0,1] neg_hi:[0,1]
	v_mul_f32_e32 v56, 0xbfb8aa3b, v65
	v_fma_f32 v57, v65, s91, -v56
	v_rndne_f32_e32 v105, v56
	v_fmac_f32_e32 v57, 0xb2a5705f, v65
	v_sub_f32_e32 v56, v56, v105
	v_add_f32_e32 v56, v56, v57
	v_exp_f32_e32 v56, v56
	v_cvt_i32_f32_e32 v57, v105
	v_pk_add_f32 v[44:45], v[34:35], v[64:65] op_sel_hi:[1,0] neg_lo:[0,1] neg_hi:[0,1]
	v_pk_add_f32 v[34:35], v[32:33], v[64:65] op_sel_hi:[1,0] neg_lo:[0,1] neg_hi:[0,1]
	v_pk_add_f32 v[32:33], v[108:109], v[64:65] op_sel_hi:[1,0] neg_lo:[0,1] neg_hi:[0,1]
	v_ldexp_f32 v56, v56, v57
	v_mul_f32_e32 v57, 0xbfb8aa3b, v103
	v_fma_f32 v105, v103, s91, -v57
	v_rndne_f32_e32 v107, v57
	v_fmac_f32_e32 v105, 0xb2a5705f, v103
	v_sub_f32_e32 v57, v57, v107
	v_add_f32_e32 v57, v57, v105
	v_exp_f32_e32 v57, v57
	v_cvt_i32_f32_e32 v105, v107
	v_cndmask_b32_e32 v56, 0, v56, vcc
	v_cmp_ngt_f32_e32 vcc, s88, v65
	v_pk_add_f32 v[54:55], v[54:55], v[64:65] op_sel_hi:[1,0] neg_lo:[0,1] neg_hi:[0,1]
	v_ldexp_f32 v57, v57, v105
	v_cndmask_b32_e32 v56, v191, v56, vcc
	v_cmp_nlt_f32_e32 vcc, s89, v103
	v_pk_mul_f32 v[68:69], v[54:55], v[54:55]
	v_pk_add_f32 v[52:53], v[52:53], v[64:65] op_sel_hi:[1,0] neg_lo:[0,1] neg_hi:[0,1]
	v_cndmask_b32_e32 v57, 0, v57, vcc
	v_cmp_ngt_f32_e32 vcc, s88, v103
	v_pk_mul_f32 v[110:111], v[52:53], v[52:53]
	v_add_f32_e32 v68, v68, v69
	v_cndmask_b32_e32 v57, v191, v57, vcc
	v_pk_add_f32 v[56:57], v[56:57], 1.0 op_sel_hi:[1,0]
	v_add_f32_e32 v68, v110, v68
	v_div_scale_f32 v105, s[0:1], v57, v57, v103
	v_rcp_f32_e32 v107, v105
	v_pk_mul_f32 v[112:113], v[44:45], v[44:45]
	v_add_f32_e32 v68, v111, v68
	v_pk_add_f32 v[42:43], v[36:37], v[64:65] op_sel_hi:[1,0] neg_lo:[0,1] neg_hi:[0,1]
	v_fma_f32 v108, -v105, v107, 1.0
	v_fmac_f32_e32 v107, v108, v107
	v_div_scale_f32 v108, vcc, v103, v57, v103
	v_mul_f32_e32 v109, v108, v107
	v_fma_f32 v192, -v105, v109, v108
	v_fmac_f32_e32 v109, v192, v107
	v_fma_f32 v105, -v105, v109, v108
	v_div_fmas_f32 v105, v105, v107, v109
	v_div_fixup_f32 v57, v105, v57, v103
	v_div_scale_f32 v103, s[0:1], v56, v56, v65
	v_rcp_f32_e32 v105, v103
	v_add_f32_e32 v68, v112, v68
	v_pk_mul_f32 v[114:115], v[42:43], v[42:43]
	v_add_f32_e32 v68, v113, v68
	v_fma_f32 v107, -v103, v105, 1.0
	v_fmac_f32_e32 v105, v107, v105
	v_div_scale_f32 v107, vcc, v65, v56, v65
	v_mul_f32_e32 v108, v107, v105
	v_fma_f32 v109, -v103, v108, v107
	v_fmac_f32_e32 v108, v109, v105
	v_fma_f32 v103, -v103, v108, v107
	v_div_fmas_f32 v103, v103, v105, v108
	v_div_fixup_f32 v56, v103, v56, v65
	v_pk_add_f32 v[64:65], v[66:67], v[64:65] op_sel_hi:[1,0] neg_lo:[0,1] neg_hi:[0,1]
	v_add_f32_e32 v68, v114, v68
	v_pk_mul_f32 v[66:67], v[64:65], v[64:65]
	v_add_f32_e32 v68, v115, v68
	v_add_f32_e32 v66, v66, v68
	v_pk_mul_f32 v[36:37], v[38:39], v[38:39]
	v_add_f32_e32 v66, v67, v66
	v_add_f32_e32 v36, v36, v66
	v_pk_mul_f32 v[58:59], v[34:35], v[34:35]
	v_add_f32_e32 v36, v37, v36
	v_add_f32_e32 v36, v58, v36
	v_pk_mul_f32 v[60:61], v[32:33], v[32:33]
	v_add_f32_e32 v36, v59, v36
	v_add_f32_e32 v36, v60, v36
	v_add_f32_e32 v36, v61, v36
	ds_bpermute_b32 v37, v116, v36
	s_mov_b32 s0, 0xf800000
	v_mov_b64 v[108:109], v[220:221]
	s_waitcnt lgkmcnt(0)
	v_add_f32_e32 v36, v36, v37
	ds_bpermute_b32 v37, v117, v36
	s_waitcnt lgkmcnt(0)
	v_add_f32_e32 v36, v36, v37
	v_fmamk_f32 v36, v36, 0x3c800000, v189
	v_cmp_gt_f32_e32 vcc, s0, v36
	v_mul_f32_e32 v37, 0x4f800000, v36
	s_nop 0
	v_cndmask_b32_e32 v36, v36, v37, vcc
	v_sqrt_f32_e32 v37, v36
	s_nop 0
	v_add_u32_e32 v58, -1, v37
	v_fma_f32 v59, -v58, v37, v36
	v_cmp_ge_f32_e64 s[0:1], 0, v59
	v_add_u32_e32 v59, 1, v37
	s_nop 0
	v_cndmask_b32_e64 v58, v37, v58, s[0:1]
	v_fma_f32 v37, -v59, v37, v36
	v_cmp_lt_f32_e64 s[0:1], 0, v37
	s_nop 1
	v_cndmask_b32_e64 v37, v58, v59, s[0:1]
	v_mul_f32_e32 v58, 0x37800000, v37
	v_cndmask_b32_e32 v37, v37, v58, vcc
	v_cmp_class_f32_e32 vcc, v36, v190
	s_nop 1
	v_cndmask_b32_e32 v36, v37, v36, vcc
	v_div_scale_f32 v37, s[0:1], v36, v36, 1.0
	v_rcp_f32_e32 v58, v37
	s_nop 0
	v_fma_f32 v59, -v37, v58, 1.0
	v_fmac_f32_e32 v58, v59, v58
	v_div_scale_f32 v59, vcc, 1.0, v36, 1.0
	v_mul_f32_e32 v60, v59, v58
	v_fma_f32 v61, -v37, v60, v59
	v_fmac_f32_e32 v60, v61, v58
	v_fma_f32 v37, -v37, v60, v59
	v_div_fmas_f32 v37, v37, v58, v60
	v_div_fixup_f32 v36, v37, v36, 1.0
	v_pk_mul_f32 v[54:55], v[54:55], v[36:37] op_sel_hi:[1,0]
	v_pk_mul_f32 v[44:45], v[44:45], v[36:37] op_sel_hi:[1,0]
	v_pk_mul_f32 v[26:27], v[26:27], v[54:55]
	s_nop 0
	v_pk_mul_f32 v[26:27], v[50:51], v[26:27]
	v_pk_mul_f32 v[50:51], v[52:53], v[36:37] op_sel_hi:[1,0]
	v_cvt_pk_bf16_f32 v26, v26, v27
	v_pk_mul_f32 v[28:29], v[28:29], v[50:51]
	s_nop 0
	v_pk_mul_f32 v[28:29], v[48:49], v[28:29]
	s_nop 0
	v_cvt_pk_bf16_f32 v27, v28, v29
	global_store_dwordx2 v[30:31], v[26:27], off
	s_nop 1
	v_mov_b64 v[26:27], v[204:205]
	v_mov_b64 v[28:29], v[206:207]
	v_pk_mul_f32 v[26:27], v[26:27], v[44:45]
	s_nop 0
	v_pk_mul_f32 v[26:27], v[40:41], v[26:27]
	v_pk_mul_f32 v[40:41], v[42:43], v[36:37] op_sel_hi:[1,0]
	v_cvt_pk_bf16_f32 v26, v26, v27
	v_pk_mul_f32 v[28:29], v[28:29], v[40:41]
	v_lshlrev_b32_e32 v37, 16, v108
	v_pk_mul_f32 v[28:29], v[56:57], v[28:29]
	v_mul_f32_e32 v40, 0xbfb8aa3b, v37
	v_cvt_pk_bf16_f32 v27, v28, v29
	global_store_dwordx2 v[30:31], v[26:27], off offset:32
	s_nop 1
	v_mov_b64 v[26:27], v[208:209]
	v_mov_b64 v[28:29], v[210:211]
	v_fma_f32 v41, v37, s91, -v40
	v_rndne_f32_e32 v43, v40
	v_fmac_f32_e32 v41, 0xb2a5705f, v37
	v_sub_f32_e32 v40, v40, v43
	v_add_f32_e32 v40, v40, v41
	v_exp_f32_e32 v40, v40
	v_cvt_i32_f32_e32 v41, v43
	v_and_b32_e32 v42, 0xffff0000, v108
	v_cmp_nlt_f32_e32 vcc, s89, v37
	v_ldexp_f32 v40, v40, v41
	v_mul_f32_e32 v41, 0xbfb8aa3b, v42
	v_fma_f32 v43, v42, s91, -v41
	v_rndne_f32_e32 v44, v41
	v_fmac_f32_e32 v43, 0xb2a5705f, v42
	v_sub_f32_e32 v41, v41, v44
	v_add_f32_e32 v41, v41, v43
	v_exp_f32_e32 v41, v41
	v_cvt_i32_f32_e32 v43, v44
	v_cndmask_b32_e32 v40, 0, v40, vcc
	v_cmp_ngt_f32_e32 vcc, s88, v37
	v_ldexp_f32 v41, v41, v43
	s_nop 0
	v_cndmask_b32_e32 v40, v191, v40, vcc
	v_cmp_nlt_f32_e32 vcc, s89, v42
	s_nop 1
	v_cndmask_b32_e32 v41, 0, v41, vcc
	v_cmp_ngt_f32_e32 vcc, s88, v42
	s_nop 1
	v_cndmask_b32_e32 v41, v191, v41, vcc
	v_pk_add_f32 v[40:41], v[40:41], 1.0 op_sel_hi:[1,0]
	s_nop 0
	v_div_scale_f32 v43, s[0:1], v41, v41, v42
	v_rcp_f32_e32 v44, v43
	s_nop 0
	v_fma_f32 v45, -v43, v44, 1.0
	v_fmac_f32_e32 v44, v45, v44
	v_div_scale_f32 v45, vcc, v42, v41, v42
	v_mul_f32_e32 v48, v45, v44
	v_fma_f32 v49, -v43, v48, v45
	v_fmac_f32_e32 v48, v49, v44
	v_fma_f32 v43, -v43, v48, v45
	v_div_fmas_f32 v43, v43, v44, v48
	v_div_fixup_f32 v41, v43, v41, v42
	v_div_scale_f32 v42, s[0:1], v40, v40, v37
	v_rcp_f32_e32 v43, v42
	s_nop 0
	v_fma_f32 v44, -v42, v43, 1.0
	v_fmac_f32_e32 v43, v44, v43
	v_div_scale_f32 v44, vcc, v37, v40, v37
	v_mul_f32_e32 v45, v44, v43
	v_fma_f32 v48, -v42, v45, v44
	v_fmac_f32_e32 v45, v48, v43
	v_fma_f32 v42, -v42, v45, v44
	v_div_fmas_f32 v42, v42, v43, v45
	v_div_fixup_f32 v40, v42, v40, v37
	v_pk_mul_f32 v[42:43], v[64:65], v[36:37] op_sel_hi:[1,0]
	v_lshlrev_b32_e32 v37, 16, v109
	v_cmp_nlt_f32_e32 vcc, s89, v37
	v_pk_mul_f32 v[38:39], v[38:39], v[36:37] op_sel_hi:[1,0]
	v_pk_mul_f32 v[26:27], v[26:27], v[42:43]
	s_nop 0
	v_pk_mul_f32 v[26:27], v[40:41], v[26:27]
	v_mul_f32_e32 v40, 0xbfb8aa3b, v37
	v_fma_f32 v41, v37, s91, -v40
	v_rndne_f32_e32 v43, v40
	v_fmac_f32_e32 v41, 0xb2a5705f, v37
	v_sub_f32_e32 v40, v40, v43
	v_add_f32_e32 v40, v40, v41
	v_exp_f32_e32 v40, v40
	v_cvt_i32_f32_e32 v41, v43
	v_and_b32_e32 v42, 0xffff0000, v109
	v_pk_mul_f32 v[28:29], v[28:29], v[38:39]
	v_cvt_pk_bf16_f32 v26, v26, v27
	v_ldexp_f32 v40, v40, v41
	v_mul_f32_e32 v41, 0xbfb8aa3b, v42
	v_fma_f32 v43, v42, s91, -v41
	v_rndne_f32_e32 v44, v41
	v_fmac_f32_e32 v43, 0xb2a5705f, v42
	v_sub_f32_e32 v41, v41, v44
	v_add_f32_e32 v41, v41, v43
	v_exp_f32_e32 v41, v41
	v_cvt_i32_f32_e32 v43, v44
	v_cndmask_b32_e32 v40, 0, v40, vcc
	v_cmp_ngt_f32_e32 vcc, s88, v37
	v_ldexp_f32 v41, v41, v43
	s_nop 0
	v_cndmask_b32_e32 v40, v191, v40, vcc
	v_cmp_nlt_f32_e32 vcc, s89, v42
	s_nop 1
	v_cndmask_b32_e32 v41, 0, v41, vcc
	v_cmp_ngt_f32_e32 vcc, s88, v42
	s_nop 1
	v_cndmask_b32_e32 v41, v191, v41, vcc
	v_pk_add_f32 v[40:41], v[40:41], 1.0 op_sel_hi:[1,0]
	s_nop 0
	v_div_scale_f32 v43, s[0:1], v41, v41, v42
	v_rcp_f32_e32 v44, v43
	s_nop 0
	v_fma_f32 v45, -v43, v44, 1.0
	v_fmac_f32_e32 v44, v45, v44
	v_div_scale_f32 v45, vcc, v42, v41, v42
	v_mul_f32_e32 v48, v45, v44
	v_fma_f32 v49, -v43, v48, v45
	v_fmac_f32_e32 v48, v49, v44
	v_fma_f32 v43, -v43, v48, v45
	v_div_fmas_f32 v43, v43, v44, v48
	v_div_fixup_f32 v41, v43, v41, v42
	v_div_scale_f32 v42, s[0:1], v40, v40, v37
	v_rcp_f32_e32 v43, v42
	s_nop 0
	v_fma_f32 v44, -v42, v43, 1.0
	v_fmac_f32_e32 v43, v44, v43
	v_div_scale_f32 v44, vcc, v37, v40, v37
	v_mul_f32_e32 v45, v44, v43
	v_fma_f32 v48, -v42, v45, v44
	v_fmac_f32_e32 v45, v48, v43
	v_fma_f32 v42, -v42, v45, v44
	v_div_fmas_f32 v42, v42, v43, v45
	v_div_fixup_f32 v40, v42, v40, v37
	v_pk_mul_f32 v[28:29], v[40:41], v[28:29]
	s_nop 0
	v_cvt_pk_bf16_f32 v27, v28, v29
	global_store_dwordx2 v[30:31], v[26:27], off offset:64
	v_mov_b64 v[38:39], v[230:231]
	s_nop 0
	s_nop 1
	v_mov_b64 v[26:27], v[212:213]
	v_mov_b64 v[28:29], v[214:215]
	v_lshlrev_b32_e32 v37, 16, v38
	v_mul_f32_e32 v40, 0xbfb8aa3b, v37
	v_fma_f32 v41, v37, s91, -v40
	v_rndne_f32_e32 v42, v40
	v_fmac_f32_e32 v41, 0xb2a5705f, v37
	v_sub_f32_e32 v40, v40, v42
	v_add_f32_e32 v40, v40, v41
	v_exp_f32_e32 v40, v40
	v_cvt_i32_f32_e32 v41, v42
	v_and_b32_e32 v38, 0xffff0000, v38
	v_cmp_nlt_f32_e32 vcc, s89, v37
	v_pk_mul_f32 v[34:35], v[34:35], v[36:37] op_sel_hi:[1,0]
	v_ldexp_f32 v40, v40, v41
	v_mul_f32_e32 v41, 0xbfb8aa3b, v38
	v_fma_f32 v42, v38, s91, -v41
	v_rndne_f32_e32 v43, v41
	v_fmac_f32_e32 v42, 0xb2a5705f, v38
	v_sub_f32_e32 v41, v41, v43
	v_add_f32_e32 v41, v41, v42
	v_exp_f32_e32 v41, v41
	v_cvt_i32_f32_e32 v42, v43
	v_cndmask_b32_e32 v40, 0, v40, vcc
	v_cmp_ngt_f32_e32 vcc, s88, v37
	v_pk_mul_f32 v[26:27], v[26:27], v[34:35]
	v_ldexp_f32 v41, v41, v42
	v_cndmask_b32_e32 v40, v191, v40, vcc
	v_cmp_nlt_f32_e32 vcc, s89, v38
	s_nop 1
	v_cndmask_b32_e32 v41, 0, v41, vcc
	v_cmp_ngt_f32_e32 vcc, s88, v38
	s_nop 1
	v_cndmask_b32_e32 v41, v191, v41, vcc
	v_pk_add_f32 v[40:41], v[40:41], 1.0 op_sel_hi:[1,0]
	s_nop 0
	v_div_scale_f32 v42, s[0:1], v41, v41, v38
	v_rcp_f32_e32 v43, v42
	s_nop 0
	v_fma_f32 v44, -v42, v43, 1.0
	v_fmac_f32_e32 v43, v44, v43
	v_div_scale_f32 v44, vcc, v38, v41, v38
	v_mul_f32_e32 v45, v44, v43
	v_fma_f32 v46, -v42, v45, v44
	v_fmac_f32_e32 v45, v46, v43
	v_fma_f32 v42, -v42, v45, v44
	v_div_fmas_f32 v42, v42, v43, v45
	v_div_fixup_f32 v41, v42, v41, v38
	v_div_scale_f32 v38, s[0:1], v40, v40, v37
	v_rcp_f32_e32 v42, v38
	s_nop 0
	v_fma_f32 v43, -v38, v42, 1.0
	v_fmac_f32_e32 v42, v43, v42
	v_div_scale_f32 v43, vcc, v37, v40, v37
	v_mul_f32_e32 v44, v43, v42
	v_fma_f32 v45, -v38, v44, v43
	v_fmac_f32_e32 v44, v45, v42
	v_fma_f32 v38, -v38, v44, v43
	v_div_fmas_f32 v38, v38, v42, v44
	v_div_fixup_f32 v40, v38, v40, v37
	v_lshlrev_b32_e32 v37, 16, v39
	v_mul_f32_e32 v34, 0xbfb8aa3b, v37
	v_and_b32_e32 v38, 0xffff0000, v39
	v_fma_f32 v35, v37, s91, -v34
	v_rndne_f32_e32 v39, v34
	v_fmac_f32_e32 v35, 0xb2a5705f, v37
	v_sub_f32_e32 v34, v34, v39
	v_add_f32_e32 v34, v34, v35
	v_exp_f32_e32 v34, v34
	v_cvt_i32_f32_e32 v35, v39
	v_pk_mul_f32 v[26:27], v[40:41], v[26:27]
	v_cmp_nlt_f32_e32 vcc, s89, v37
	v_pk_mul_f32 v[32:33], v[32:33], v[36:37] op_sel_hi:[1,0]
	v_ldexp_f32 v34, v34, v35
	v_mul_f32_e32 v35, 0xbfb8aa3b, v38
	v_fma_f32 v39, v38, s91, -v35
	v_rndne_f32_e32 v40, v35
	v_fmac_f32_e32 v39, 0xb2a5705f, v38
	v_sub_f32_e32 v35, v35, v40
	v_add_f32_e32 v35, v35, v39
	v_exp_f32_e32 v35, v35
	v_cvt_i32_f32_e32 v39, v40
	v_cndmask_b32_e32 v34, 0, v34, vcc
	v_cmp_ngt_f32_e32 vcc, s88, v37
	v_pk_mul_f32 v[28:29], v[28:29], v[32:33]
	v_ldexp_f32 v35, v35, v39
	v_cndmask_b32_e32 v34, v191, v34, vcc
	v_cmp_nlt_f32_e32 vcc, s89, v38
	v_cvt_pk_bf16_f32 v26, v26, v27
	s_nop 0
	v_cndmask_b32_e32 v35, 0, v35, vcc
	v_cmp_ngt_f32_e32 vcc, s88, v38
	s_nop 1
	v_cndmask_b32_e32 v35, v191, v35, vcc
	v_pk_add_f32 v[34:35], v[34:35], 1.0 op_sel_hi:[1,0]
	s_nop 0
	v_div_scale_f32 v39, s[0:1], v35, v35, v38
	v_rcp_f32_e32 v40, v39
	s_nop 0
	v_fma_f32 v41, -v39, v40, 1.0
	v_fmac_f32_e32 v40, v41, v40
	v_div_scale_f32 v41, vcc, v38, v35, v38
	v_mul_f32_e32 v42, v41, v40
	v_fma_f32 v43, -v39, v42, v41
	v_fmac_f32_e32 v42, v43, v40
	v_fma_f32 v39, -v39, v42, v41
	v_div_fmas_f32 v39, v39, v40, v42
	v_div_fixup_f32 v35, v39, v35, v38
	v_div_scale_f32 v38, s[0:1], v34, v34, v37
	v_rcp_f32_e32 v39, v38
	s_nop 0
	v_fma_f32 v40, -v38, v39, 1.0
	v_fmac_f32_e32 v39, v40, v39
	v_div_scale_f32 v40, vcc, v37, v34, v37
	v_mul_f32_e32 v41, v40, v39
	v_fma_f32 v42, -v38, v41, v40
	v_fmac_f32_e32 v41, v42, v39
	v_fma_f32 v38, -v38, v41, v40
	v_div_fmas_f32 v38, v38, v39, v41
	v_div_fixup_f32 v34, v38, v34, v37
	v_pk_mul_f32 v[28:29], v[34:35], v[28:29]
	s_andn2_b64 vcc, exec, s[84:85]
	v_cvt_pk_bf16_f32 v27, v28, v29
	global_store_dwordx2 v[30:31], v[26:27], off offset:96
	s_cbranch_vccz .LBB0_1286

.LBB0_3593:
	ds_read_b128 v[30:33], v183
	ds_read_b128 v[26:29], v183 offset:64
	ds_read_b128 v[34:37], v184 offset:18432
	ds_read_b128 v[38:41], v184 offset:18496
	s_lshl_b32 s0, s93, 5
	s_sub_i32 s2, s86, s0
	s_lshr_b32 s0, s92, 24
	s_waitcnt lgkmcnt(1)
	v_mfma_f32_16x16x32_bf16 v[34:37], v[34:37], v[30:33], 0
	s_add_i32 s0, s86, s0
	s_ashr_i32 s0, s0, 8
	s_ashr_i32 s1, s0, 31
	s_waitcnt lgkmcnt(0)
	v_mfma_f32_16x16x32_bf16 v[54:57], v[38:41], v[26:29], v[34:37]
	ds_read_b128 v[38:41], v184 offset:20800
	s_ashr_i32 s3, s2, 31
	s_nop 0
	ds_read_b128 v[34:37], v184 offset:20736
	s_lshl_b64 s[0:1], s[0:1], 12
	s_lshl_b64 s[92:93], s[2:3], 7
	s_add_u32 s0, s0, s92
	s_addc_u32 s1, s1, s93
	s_waitcnt lgkmcnt(0)
	v_mfma_f32_16x16x32_bf16 v[34:37], v[34:37], v[30:33], 0
	s_lshl_b32 s86, s97, 7
	v_lshl_add_u64 v[212:213], s[0:1], 0, v[82:83]
	v_mov_b64_e32 v[238:239], s[84:85]
	v_mad_u64_u32 v[238:239], s[98:99], v212, s95, v[238:239]
	v_mad_i32_i24 v239, v213, s95, v239
	v_lshl_add_u64 v[238:239], v[238:239], 0, s[86:87]
	v_lshl_add_u64 v[238:239], v[238:239], 0, v[72:73]
	global_load_dwordx2 v[216:217], v[238:239], off offset:3072
	global_load_dwordx2 v[218:219], v[238:239], off offset:3104
	global_load_dwordx2 v[220:221], v[238:239], off offset:3136
	global_load_dwordx2 v[230:231], v[238:239], off offset:3168
	v_lshl_add_u64 v[238:239], v[84:85], 0, s[86:87]
	v_lshl_add_u64 v[238:239], v[238:239], 0, s[86:87]
	global_load_dwordx4 v[200:203], v[238:239], off
	global_load_dwordx4 v[204:207], v[238:239], off offset:64
	global_load_dwordx4 v[208:211], v[238:239], off offset:128
	global_load_dwordx4 v[212:215], v[238:239], off offset:192
	ds_read_b128 v[58:61], v184 offset:34624
	v_mfma_f32_16x16x32_bf16 v[62:65], v[38:41], v[26:29], v[34:37]
	ds_read_b128 v[38:41], v184 offset:23104
	s_nop 3
	ds_read_b128 v[34:37], v184 offset:23040
	s_waitcnt lgkmcnt(0)
	v_mfma_f32_16x16x32_bf16 v[34:37], v[34:37], v[30:33], 0
	v_mfma_f32_16x16x32_bf16 v[66:69], v[38:41], v[26:29], v[34:37]
	ds_read_b128 v[38:41], v184 offset:25408
	s_nop 5
	ds_read_b128 v[34:37], v184 offset:25344
	s_waitcnt lgkmcnt(0)
	v_mfma_f32_16x16x32_bf16 v[34:37], v[34:37], v[30:33], 0
	v_mfma_f32_16x16x32_bf16 v[50:53], v[38:41], v[26:29], v[34:37]
	ds_read_b128 v[38:41], v184 offset:27712
	s_nop 5
	ds_read_b128 v[34:37], v184 offset:27648
	s_waitcnt lgkmcnt(0)
	v_mfma_f32_16x16x32_bf16 v[34:37], v[34:37], v[30:33], 0
	v_mfma_f32_16x16x32_bf16 v[46:49], v[38:41], v[26:29], v[34:37]
	ds_read_b128 v[38:41], v184 offset:30016
	s_nop 5
	ds_read_b128 v[34:37], v184 offset:29952
	s_waitcnt lgkmcnt(0)
	v_mfma_f32_16x16x32_bf16 v[34:37], v[34:37], v[30:33], 0
	v_mfma_f32_16x16x32_bf16 v[42:45], v[38:41], v[26:29], v[34:37]
	ds_read_b128 v[38:41], v184 offset:32320
	s_nop 5
	ds_read_b128 v[34:37], v184 offset:32256
	s_waitcnt lgkmcnt(0)
	v_mfma_f32_16x16x32_bf16 v[34:37], v[34:37], v[30:33], 0
	v_mfma_f32_16x16x32_bf16 v[38:41], v[38:41], v[26:29], v[34:37]
	s_nop 6
	ds_read_b128 v[34:37], v184 offset:34560
	s_waitcnt lgkmcnt(0)
	v_mfma_f32_16x16x32_bf16 v[34:37], v[34:37], v[30:33], 0
	v_mfma_f32_16x16x32_bf16 v[34:37], v[58:61], v[26:29], v[34:37]
	v_mul_f32_e32 v58, v107, v89
	v_mul_f32_e32 v59, v108, v87
	v_cndmask_b32_e64 v58, v59, v58, s[6:7]
	v_mul_f32_e32 v59, v107, v91
	v_mul_f32_e32 v60, v108, v93
	v_cndmask_b32_e64 v59, v59, v60, s[12:13]
	v_mul_f32_e32 v58, 0x3fb8aa3b, v58
	v_mul_f32_e32 v59, 0x3fb8aa3b, v59
	v_exp_f32_e32 v58, v58
	v_exp_f32_e32 v59, v59
	v_mul_f32_e32 v60, v108, v120
	v_pk_mul_f32 v[58:59], v[58:59], v[54:55]
	v_mul_f32_e32 v54, v107, v119
	v_mul_f32_e32 v55, v108, v118
	v_cndmask_b32_e64 v54, v55, v54, s[14:15]
	v_mul_f32_e32 v55, v107, v121
	v_cndmask_b32_e64 v55, v60, v55, s[16:17]
	v_mul_f32_e32 v54, 0x3fb8aa3b, v54
	v_mul_f32_e32 v55, 0x3fb8aa3b, v55
	v_exp_f32_e32 v54, v54
	v_exp_f32_e32 v55, v55
	v_cvt_pk_bf16_f32 v58, v58, v59
	v_pk_mul_f32 v[60:61], v[54:55], v[56:57]
	v_mul_f32_e32 v54, v107, v123
	v_mul_f32_e32 v55, v108, v122
	v_cndmask_b32_e64 v54, v55, v54, s[18:19]
	v_mul_f32_e32 v55, v107, v125
	v_mul_f32_e32 v56, v108, v124
	v_cndmask_b32_e64 v55, v56, v55, s[20:21]
	v_mul_f32_e32 v54, 0x3fb8aa3b, v54
	v_mul_f32_e32 v55, 0x3fb8aa3b, v55
	v_exp_f32_e32 v54, v54
	v_exp_f32_e32 v55, v55
	v_mul_f32_e32 v56, v108, v128
	v_mul_f32_e32 v57, v108, v134
	v_cvt_pk_bf16_f32 v59, v60, v61
	v_pk_mul_f32 v[62:63], v[54:55], v[62:63]
	v_mul_f32_e32 v54, v107, v127
	v_mul_f32_e32 v55, v108, v126
	v_cndmask_b32_e64 v54, v55, v54, s[22:23]
	v_mul_f32_e32 v55, v107, v129
	v_cndmask_b32_e64 v55, v56, v55, s[24:25]
	v_mul_f32_e32 v54, 0x3fb8aa3b, v54
	v_mul_f32_e32 v55, 0x3fb8aa3b, v55
	v_exp_f32_e32 v54, v54
	v_exp_f32_e32 v55, v55
	v_mul_f32_e32 v56, v108, v132
	v_cvt_pk_bf16_f32 v60, v62, v63
	v_pk_mul_f32 v[64:65], v[54:55], v[64:65]
	v_mul_f32_e32 v54, v107, v131
	v_mul_f32_e32 v55, v108, v130
	v_cndmask_b32_e64 v54, v55, v54, s[26:27]
	v_mul_f32_e32 v55, v107, v133
	v_cndmask_b32_e64 v55, v56, v55, s[28:29]
	v_mul_f32_e32 v54, 0x3fb8aa3b, v54
	v_mul_f32_e32 v55, 0x3fb8aa3b, v55
	v_exp_f32_e32 v54, v54
	v_exp_f32_e32 v55, v55
	v_mul_f32_e32 v56, v107, v135
	v_cndmask_b32_e64 v56, v57, v56, s[30:31]
	v_mul_f32_e32 v57, v107, v137
	v_pk_mul_f32 v[54:55], v[54:55], v[66:67]
	v_mul_f32_e32 v66, v108, v136
	v_cndmask_b32_e64 v57, v66, v57, s[34:35]
	v_mul_f32_e32 v56, 0x3fb8aa3b, v56
	v_mul_f32_e32 v57, 0x3fb8aa3b, v57
	v_exp_f32_e32 v56, v56
	v_exp_f32_e32 v57, v57
	v_mul_f32_e32 v66, v107, v139
	v_mul_f32_e32 v67, v108, v138
	v_cndmask_b32_e64 v66, v67, v66, s[36:37]
	v_pk_mul_f32 v[56:57], v[56:57], v[68:69]
	v_mul_f32_e32 v67, v107, v141
	v_mul_f32_e32 v68, v108, v140
	v_cndmask_b32_e64 v67, v68, v67, s[38:39]
	v_mul_f32_e32 v66, 0x3fb8aa3b, v66
	v_mul_f32_e32 v67, 0x3fb8aa3b, v67
	v_exp_f32_e32 v66, v66
	v_exp_f32_e32 v67, v67
	v_mul_f32_e32 v68, v108, v144
	v_cvt_pk_bf16_f32 v61, v64, v65
	v_cvt_pk_bf16_f32 v54, v54, v55
	v_pk_mul_f32 v[50:51], v[66:67], v[50:51]
	v_mul_f32_e32 v66, v107, v143
	v_mul_f32_e32 v67, v108, v142
	v_cndmask_b32_e64 v66, v67, v66, s[40:41]
	v_mul_f32_e32 v67, v107, v145
	v_cndmask_b32_e64 v67, v68, v67, s[42:43]
	v_mul_f32_e32 v66, 0x3fb8aa3b, v66
	v_mul_f32_e32 v67, 0x3fb8aa3b, v67
	v_exp_f32_e32 v66, v66
	v_exp_f32_e32 v67, v67
	v_mul_f32_e32 v68, v108, v148
	v_cvt_pk_bf16_f32 v55, v56, v57
	v_cvt_pk_bf16_f32 v56, v50, v51
	v_pk_mul_f32 v[52:53], v[66:67], v[52:53]
	v_mul_f32_e32 v66, v107, v147
	v_mul_f32_e32 v67, v108, v146
	v_cndmask_b32_e64 v66, v67, v66, s[44:45]
	v_mul_f32_e32 v67, v107, v149
	v_cndmask_b32_e64 v67, v68, v67, s[46:47]
	v_mul_f32_e32 v66, 0x3fb8aa3b, v66
	v_mul_f32_e32 v67, 0x3fb8aa3b, v67
	v_exp_f32_e32 v66, v66
	v_exp_f32_e32 v67, v67
	v_mul_f32_e32 v68, v108, v152
	v_cvt_pk_bf16_f32 v57, v52, v53
	v_pk_mul_f32 v[46:47], v[66:67], v[46:47]
	v_mul_f32_e32 v66, v107, v151
	v_mul_f32_e32 v67, v108, v150
	v_cndmask_b32_e64 v66, v67, v66, s[48:49]
	v_mul_f32_e32 v67, v107, v153
	v_cndmask_b32_e64 v67, v68, v67, s[50:51]
	v_mul_f32_e32 v66, 0x3fb8aa3b, v66
	v_mul_f32_e32 v67, 0x3fb8aa3b, v67
	v_exp_f32_e32 v66, v66
	v_exp_f32_e32 v67, v67
	v_mul_f32_e32 v68, v108, v156
	v_cvt_pk_bf16_f32 v46, v46, v47
	v_pk_mul_f32 v[48:49], v[66:67], v[48:49]
	v_mul_f32_e32 v66, v107, v155
	v_mul_f32_e32 v67, v108, v154
	v_cndmask_b32_e64 v66, v67, v66, s[52:53]
	v_mul_f32_e32 v67, v107, v157
	v_cndmask_b32_e64 v67, v68, v67, s[54:55]
	v_mul_f32_e32 v66, 0x3fb8aa3b, v66
	v_mul_f32_e32 v67, 0x3fb8aa3b, v67
	v_exp_f32_e32 v66, v66
	v_exp_f32_e32 v67, v67
	v_mul_f32_e32 v68, v108, v160
	v_cvt_pk_bf16_f32 v47, v48, v49
	v_pk_mul_f32 v[42:43], v[66:67], v[42:43]
	v_mul_f32_e32 v66, v107, v159
	v_mul_f32_e32 v67, v108, v158
	v_cndmask_b32_e64 v66, v67, v66, s[56:57]
	v_mul_f32_e32 v67, v107, v161
	v_cndmask_b32_e64 v67, v68, v67, s[58:59]
	v_mul_f32_e32 v66, 0x3fb8aa3b, v66
	v_mul_f32_e32 v67, 0x3fb8aa3b, v67
	v_exp_f32_e32 v66, v66
	v_exp_f32_e32 v67, v67
	v_mul_f32_e32 v68, v108, v164
	v_cvt_pk_bf16_f32 v48, v42, v43
	v_pk_mul_f32 v[44:45], v[66:67], v[44:45]
	v_mul_f32_e32 v66, v107, v163
	v_mul_f32_e32 v67, v108, v162
	v_cndmask_b32_e64 v66, v67, v66, s[60:61]
	v_mul_f32_e32 v67, v107, v165
	v_cndmask_b32_e64 v67, v68, v67, s[62:63]
	v_mul_f32_e32 v66, 0x3fb8aa3b, v66
	v_mul_f32_e32 v67, 0x3fb8aa3b, v67
	v_exp_f32_e32 v66, v66
	v_exp_f32_e32 v67, v67
	v_mul_f32_e32 v68, v108, v168
	v_cvt_pk_bf16_f32 v49, v44, v45
	v_pk_mul_f32 v[38:39], v[66:67], v[38:39]
	v_mul_f32_e32 v66, v107, v167
	v_mul_f32_e32 v67, v108, v166
	v_cndmask_b32_e64 v66, v67, v66, s[64:65]
	v_mul_f32_e32 v67, v107, v169
	v_cndmask_b32_e64 v67, v68, v67, s[66:67]
	v_mul_f32_e32 v66, 0x3fb8aa3b, v66
	v_mul_f32_e32 v67, 0x3fb8aa3b, v67
	v_exp_f32_e32 v66, v66
	v_exp_f32_e32 v67, v67
	v_mul_f32_e32 v68, v108, v172
	v_cvt_pk_bf16_f32 v38, v38, v39
	v_pk_mul_f32 v[40:41], v[66:67], v[40:41]
	v_mul_f32_e32 v66, v107, v171
	v_mul_f32_e32 v67, v108, v170
	v_cndmask_b32_e64 v66, v67, v66, s[68:69]
	v_mul_f32_e32 v67, v107, v173
	v_cndmask_b32_e64 v67, v68, v67, s[70:71]
	v_mul_f32_e32 v66, 0x3fb8aa3b, v66
	v_mul_f32_e32 v67, 0x3fb8aa3b, v67
	v_exp_f32_e32 v66, v66
	v_exp_f32_e32 v67, v67
	v_mul_f32_e32 v68, v108, v176
	v_cvt_pk_bf16_f32 v39, v40, v41
	v_pk_mul_f32 v[34:35], v[66:67], v[34:35]
	v_mul_f32_e32 v66, v107, v175
	v_mul_f32_e32 v67, v108, v174
	v_cndmask_b32_e64 v66, v67, v66, s[72:73]
	v_mul_f32_e32 v67, v107, v177
	v_cndmask_b32_e64 v67, v68, v67, s[74:75]
	v_mul_f32_e32 v66, 0x3fb8aa3b, v66
	v_mul_f32_e32 v67, 0x3fb8aa3b, v67
	v_exp_f32_e32 v66, v66
	v_exp_f32_e32 v67, v67
	v_cvt_pk_bf16_f32 v40, v34, v35
	v_pk_mul_f32 v[36:37], v[66:67], v[36:37]
	ds_read_b64_tr_b16 v[64:65], v185 offset:39168
	ds_read_b64_tr_b16 v[62:63], v185 offset:36864
	ds_read_b64_tr_b16 v[66:67], v185 offset:36896
	ds_read_b64_tr_b16 v[68:69], v185 offset:39200
	ds_read_b64_tr_b16 v[110:111], v185 offset:36928
	ds_read_b64_tr_b16 v[112:113], v185 offset:39232
	ds_read_b64_tr_b16 v[192:193], v185 offset:36960
	ds_read_b64_tr_b16 v[194:195], v185 offset:39264
	s_waitcnt lgkmcnt(6)
	v_mfma_f32_16x16x32_bf16 v[62:65], v[62:65], v[58:61], 0
	v_cvt_pk_bf16_f32 v41, v36, v37
	s_waitcnt lgkmcnt(4)
	v_mfma_f32_16x16x32_bf16 v[66:69], v[66:69], v[58:61], 0
	s_waitcnt lgkmcnt(2)
	v_mfma_f32_16x16x32_bf16 v[110:113], v[110:113], v[58:61], 0
	s_waitcnt lgkmcnt(0)
	v_mfma_f32_16x16x32_bf16 v[58:61], v[192:195], v[58:61], 0
	ds_read_b64_tr_b16 v[52:53], v186 offset:39168
	ds_read_b64_tr_b16 v[50:51], v186 offset:36864
	ds_read_b64_tr_b16 v[192:193], v186 offset:36896
	ds_read_b64_tr_b16 v[194:195], v186 offset:39200
	s_waitcnt lgkmcnt(2)
	v_mfma_f32_16x16x32_bf16 v[50:53], v[50:53], v[54:57], v[62:65]
	s_waitcnt lgkmcnt(0)
	v_mfma_f32_16x16x32_bf16 v[62:65], v[192:195], v[54:57], v[66:69]
	s_nop 2
	ds_read_b64_tr_b16 v[66:67], v186 offset:36928
	ds_read_b64_tr_b16 v[68:69], v186 offset:39232
	s_waitcnt lgkmcnt(0)
	v_mfma_f32_16x16x32_bf16 v[66:69], v[66:69], v[54:57], v[110:113]
	s_nop 2
	ds_read_b64_tr_b16 v[110:111], v186 offset:36960
	ds_read_b64_tr_b16 v[112:113], v186 offset:39264
	s_waitcnt lgkmcnt(0)
	v_mfma_f32_16x16x32_bf16 v[54:57], v[110:113], v[54:57], v[58:61]
	ds_read_b64_tr_b16 v[44:45], v187 offset:39168
	ds_read_b64_tr_b16 v[42:43], v187 offset:36864
	s_nop 0
	ds_read_b64_tr_b16 v[58:59], v187 offset:36896
	ds_read_b64_tr_b16 v[60:61], v187 offset:39200
	s_waitcnt lgkmcnt(2)
	v_mfma_f32_16x16x32_bf16 v[42:45], v[42:45], v[46:49], v[50:53]
	s_nop 2
	ds_read_b64_tr_b16 v[50:51], v187 offset:36928
	ds_read_b64_tr_b16 v[52:53], v187 offset:39232
	s_waitcnt lgkmcnt(2)
	v_mfma_f32_16x16x32_bf16 v[58:61], v[58:61], v[46:49], v[62:65]
	s_waitcnt lgkmcnt(0)
	v_mfma_f32_16x16x32_bf16 v[62:65], v[50:53], v[46:49], v[66:69]
	ds_read_b64_tr_b16 v[50:51], v187 offset:36960
	ds_read_b64_tr_b16 v[52:53], v187 offset:39264
	s_waitcnt lgkmcnt(0)
	v_mfma_f32_16x16x32_bf16 v[54:57], v[50:53], v[46:49], v[54:57]
	ds_read_b64_tr_b16 v[36:37], v188 offset:39168
	ds_read_b64_tr_b16 v[34:35], v188 offset:36864
	ds_read_b64_tr_b16 v[46:47], v188 offset:36896
	ds_read_b64_tr_b16 v[48:49], v188 offset:39200
	s_waitcnt lgkmcnt(2)
	v_mfma_f32_16x16x32_bf16 v[50:53], v[34:37], v[38:41], v[42:45]
	s_nop 2
	ds_read_b64_tr_b16 v[42:43], v188 offset:36928
	ds_read_b64_tr_b16 v[44:45], v188 offset:39232
	s_waitcnt lgkmcnt(2)
	v_mfma_f32_16x16x32_bf16 v[34:37], v[46:49], v[38:41], v[58:61]
	s_waitcnt lgkmcnt(0)
	v_mfma_f32_16x16x32_bf16 v[46:49], v[42:45], v[38:41], v[62:65]
	ds_read_b64_tr_b16 v[42:43], v188 offset:36960
	ds_read_b64_tr_b16 v[44:45], v188 offset:39264
	ds_read_b128 v[110:113], v178 offset:59968
	ds_read_b128 v[62:65], v178 offset:57664
	s_waitcnt lgkmcnt(2)
	v_mfma_f32_16x16x32_bf16 v[192:195], v[42:45], v[38:41], v[54:57]
	ds_read_b128 v[38:41], v178 offset:55296
	s_nop 1
	ds_read_b128 v[54:57], v178 offset:55360
	ds_read_b128 v[42:45], v178 offset:64512
	s_waitcnt lgkmcnt(2)
	v_mfma_f32_16x16x32_bf16 v[38:41], v[38:41], v[30:33], 0
	ds_read_b128 v[66:69], v180 offset:64512
	ds_read_b128 v[196:199], v181 offset:64512
	s_waitcnt lgkmcnt(3)
	v_mfma_f32_16x16x32_bf16 v[54:57], v[54:57], v[26:29], v[38:41]
	s_nop 3
	ds_read_b128 v[38:41], v178 offset:64576
	s_waitcnt lgkmcnt(3)
	v_mfma_f32_16x16x32_bf16 v[42:45], v[42:45], v[30:33], 0
	s_waitcnt lgkmcnt(0)
	v_mfma_f32_16x16x32_bf16 v[58:61], v[38:41], v[26:29], v[42:45]
	ds_read_b128 v[38:41], v178 offset:57600
	s_nop 4
	ds_read_b128 v[42:45], v179 offset:64512
	s_waitcnt lgkmcnt(1)
	v_mfma_f32_16x16x32_bf16 v[38:41], v[38:41], v[30:33], 0
	v_mfma_f32_16x16x32_bf16 v[38:41], v[62:65], v[26:29], v[38:41]
	ds_read_b128 v[62:65], v179 offset:64576
	s_waitcnt lgkmcnt(1)
	v_mfma_f32_16x16x32_bf16 v[42:45], v[42:45], v[30:33], 0
	s_waitcnt lgkmcnt(0)
	v_mfma_f32_16x16x32_bf16 v[42:45], v[62:65], v[26:29], v[42:45]
	ds_read_b128 v[62:65], v178 offset:59904
	s_waitcnt lgkmcnt(0)
	v_mfma_f32_16x16x32_bf16 v[62:65], v[62:65], v[30:33], 0
	v_mfma_f32_16x16x32_bf16 v[62:65], v[110:113], v[26:29], v[62:65]
	ds_read_b128 v[110:113], v180 offset:64576
	v_mfma_f32_16x16x32_bf16 v[66:69], v[66:69], v[30:33], 0
	s_waitcnt lgkmcnt(0)
	v_mfma_f32_16x16x32_bf16 v[66:69], v[110:113], v[26:29], v[66:69]
	ds_read_b128 v[110:113], v178 offset:62208
	s_waitcnt lgkmcnt(0)
	v_mfma_f32_16x16x32_bf16 v[110:113], v[110:113], v[30:33], 0
	v_mfma_f32_16x16x32_bf16 v[30:33], v[196:199], v[30:33], 0
	ds_read_b128 v[196:199], v178 offset:62272
	s_waitcnt lgkmcnt(0)
	v_mfma_f32_16x16x32_bf16 v[196:199], v[196:199], v[26:29], v[110:113]
	s_nop 3
	ds_read_b128 v[110:113], v181 offset:64576
	s_waitcnt lgkmcnt(0)
	v_mfma_f32_16x16x32_bf16 v[26:29], v[110:113], v[26:29], v[30:33]
	s_nop 2
	v_mul_f32_e32 v30, v108, v1
	v_mul_f32_e32 v30, 0x3fb8aa3b, v30
	v_exp_f32_e32 v110, v30
	v_mul_f32_e32 v30, v107, v71
	v_mul_f32_e32 v30, 0x3fb8aa3b, v30
	v_exp_f32_e32 v112, v30
	s_nop 0
	v_pk_mul_f32 v[26:27], v[112:113], v[26:27] op_sel_hi:[0,1]
	v_pk_fma_f32 v[26:27], v[110:111], v[196:197], v[26:27] op_sel_hi:[0,1,1]
	v_pk_add_f32 v[32:33], v[192:193], v[26:27]
	v_pk_mul_f32 v[26:27], v[112:113], v[28:29] op_sel_hi:[0,1]
	v_pk_fma_f32 v[26:27], v[110:111], v[198:199], v[26:27] op_sel_hi:[0,1,1]
	v_pk_add_f32 v[108:109], v[194:195], v[26:27]
	v_lshl_add_u64 v[26:27], s[0:1], 0, v[82:83]
	v_mov_b64_e32 v[28:29], s[84:85]
	v_mad_u64_u32 v[28:29], s[0:1], v26, s95, v[28:29]
	v_pk_mul_f32 v[30:31], v[112:113], v[66:67] op_sel_hi:[0,1]
	v_mad_i32_i24 v29, v27, s95, v29
	v_lshlrev_b64 v[26:27], 12, v[26:27]
	v_pk_fma_f32 v[30:31], v[110:111], v[62:63], v[30:31] op_sel_hi:[0,1,1]
	v_lshl_add_u64 v[28:29], v[28:29], 0, s[86:87]
	v_lshl_add_u64 v[26:27], s[80:81], 0, v[26:27]
	v_pk_add_f32 v[66:67], v[46:47], v[30:31]
	v_lshl_add_u64 v[46:47], v[28:29], 0, v[72:73]
	v_lshl_add_u64 v[26:27], v[26:27], 0, s[86:87]
	s_lshl_b32 s86, s97, 8
	v_lshl_add_u64 v[30:31], v[26:27], 0, v[72:73]
	v_lshl_add_u64 v[62:63], v[84:85], 0, s[86:87]
	s_waitcnt vmcnt(0)
	v_mov_b64 v[114:115], v[216:217]
	s_nop 1
	v_mov_b64 v[26:27], v[200:201]
	v_mov_b64 v[28:29], v[202:203]
	v_pk_mul_f32 v[60:61], v[112:113], v[60:61] op_sel_hi:[0,1]
	v_pk_fma_f32 v[56:57], v[110:111], v[56:57], v[60:61] op_sel_hi:[0,1,1]
	v_pk_add_f32 v[52:53], v[52:53], v[56:57]
	v_pk_mul_f32 v[56:57], v[112:113], v[58:59] op_sel_hi:[0,1]
	v_pk_fma_f32 v[54:55], v[110:111], v[54:55], v[56:57] op_sel_hi:[0,1,1]
	v_pk_add_f32 v[54:55], v[50:51], v[54:55]
	v_pk_mul_f32 v[44:45], v[112:113], v[44:45] op_sel_hi:[0,1]
	v_add_f32_e32 v50, 0, v54
	v_add_f32_e32 v56, v55, v50
	v_add_f32_e32 v56, v52, v56
	s_mov_b32 s86, s96
	v_lshlrev_b32_e32 v57, 16, v114
	v_mul_f32_e32 v50, 0xbfb8aa3b, v57
	v_fma_f32 v51, v57, s8, -v50
	v_rndne_f32_e32 v59, v50
	v_fmac_f32_e32 v51, 0xb2a5705f, v57
	v_sub_f32_e32 v50, v50, v59
	v_add_f32_e32 v50, v50, v51
	v_exp_f32_e32 v50, v50
	v_cvt_i32_f32_e32 v51, v59
	v_and_b32_e32 v58, 0xffff0000, v114
	v_cmp_nlt_f32_e32 vcc, s9, v57
	v_lshlrev_b32_e32 v60, 16, v115
	v_ldexp_f32 v50, v50, v51
	v_mul_f32_e32 v51, 0xbfb8aa3b, v58
	v_fma_f32 v59, v58, s8, -v51
	v_rndne_f32_e32 v103, v51
	v_fmac_f32_e32 v59, 0xb2a5705f, v58
	v_sub_f32_e32 v51, v51, v103
	v_add_f32_e32 v51, v51, v59
	v_exp_f32_e32 v51, v51
	v_cvt_i32_f32_e32 v59, v103
	v_cndmask_b32_e32 v50, 0, v50, vcc
	v_cmp_ngt_f32_e32 vcc, s10, v57
	v_and_b32_e32 v61, 0xffff0000, v115
	v_ldexp_f32 v51, v51, v59
	v_cndmask_b32_e32 v50, v191, v50, vcc
	v_cmp_nlt_f32_e32 vcc, s9, v58
	s_nop 1
	v_cndmask_b32_e32 v51, 0, v51, vcc
	v_cmp_ngt_f32_e32 vcc, s10, v58
	s_nop 1
	v_cndmask_b32_e32 v51, v191, v51, vcc
	v_pk_add_f32 v[50:51], v[50:51], 1.0 op_sel_hi:[1,0]
	s_nop 0
	v_div_scale_f32 v59, s[0:1], v51, v51, v58
	v_rcp_f32_e32 v103, v59
	s_nop 0
	v_fma_f32 v105, -v59, v103, 1.0
	v_fmac_f32_e32 v103, v105, v103
	v_div_scale_f32 v105, vcc, v58, v51, v58
	v_mul_f32_e32 v107, v105, v103
	v_fma_f32 v111, -v59, v107, v105
	v_fmac_f32_e32 v107, v111, v103
	v_fma_f32 v59, -v59, v107, v105
	v_div_fmas_f32 v59, v59, v103, v107
	v_div_fixup_f32 v51, v59, v51, v58
	v_div_scale_f32 v58, s[0:1], v50, v50, v57
	v_rcp_f32_e32 v59, v58
	v_pk_fma_f32 v[40:41], v[110:111], v[40:41], v[44:45] op_sel_hi:[0,1,1]
	v_pk_add_f32 v[36:37], v[36:37], v[40:41]
	v_pk_mul_f32 v[40:41], v[112:113], v[42:43] op_sel_hi:[0,1]
	v_fma_f32 v103, -v58, v59, 1.0
	v_fmac_f32_e32 v59, v103, v59
	v_div_scale_f32 v103, vcc, v57, v50, v57
	v_mul_f32_e32 v105, v103, v59
	v_fma_f32 v107, -v58, v105, v103
	v_fmac_f32_e32 v105, v107, v59
	v_fma_f32 v58, -v58, v105, v103
	v_div_fmas_f32 v58, v58, v59, v105
	v_div_fixup_f32 v50, v58, v50, v57
	v_add_f32_e32 v58, v53, v56
	v_pk_mul_f32 v[56:57], v[112:113], v[68:69] op_sel_hi:[0,1]
	v_pk_fma_f32 v[56:57], v[110:111], v[64:65], v[56:57] op_sel_hi:[0,1,1]
	v_pk_add_f32 v[56:57], v[48:49], v[56:57]
	v_mul_f32_e32 v48, 0xbfb8aa3b, v60
	v_fma_f32 v49, v60, s8, -v48
	v_rndne_f32_e32 v59, v48
	v_fmac_f32_e32 v49, 0xb2a5705f, v60
	v_sub_f32_e32 v48, v48, v59
	v_add_f32_e32 v48, v48, v49
	v_exp_f32_e32 v48, v48
	v_cvt_i32_f32_e32 v49, v59
	v_cmp_nlt_f32_e32 vcc, s9, v60
	v_pk_fma_f32 v[38:39], v[110:111], v[38:39], v[40:41] op_sel_hi:[0,1,1]
	v_pk_add_f32 v[34:35], v[34:35], v[38:39]
	v_ldexp_f32 v48, v48, v49
	v_mul_f32_e32 v49, 0xbfb8aa3b, v61
	v_fma_f32 v59, v61, s8, -v49
	v_rndne_f32_e32 v64, v49
	v_fmac_f32_e32 v59, 0xb2a5705f, v61
	v_sub_f32_e32 v49, v49, v64
	v_add_f32_e32 v49, v49, v59
	v_exp_f32_e32 v49, v49
	v_cvt_i32_f32_e32 v59, v64
	v_cndmask_b32_e32 v48, 0, v48, vcc
	v_cmp_ngt_f32_e32 vcc, s10, v60
	v_add_f32_e32 v38, v58, v34
	v_ldexp_f32 v49, v49, v59
	v_cndmask_b32_e32 v48, v191, v48, vcc
	v_cmp_nlt_f32_e32 vcc, s9, v61
	v_add_f32_e32 v42, v35, v38
	s_nop 0
	v_cndmask_b32_e32 v49, 0, v49, vcc
	v_cmp_ngt_f32_e32 vcc, s10, v61
	s_nop 1
	v_cndmask_b32_e32 v49, v191, v49, vcc
	v_pk_add_f32 v[48:49], v[48:49], 1.0 op_sel_hi:[1,0]
	s_nop 0
	v_div_scale_f32 v59, s[0:1], v49, v49, v61
	v_rcp_f32_e32 v64, v59
	s_nop 0
	v_fma_f32 v65, -v59, v64, 1.0
	v_fmac_f32_e32 v64, v65, v64
	v_div_scale_f32 v65, vcc, v61, v49, v61
	v_mul_f32_e32 v68, v65, v64
	v_fma_f32 v69, -v59, v68, v65
	v_fmac_f32_e32 v68, v69, v64
	v_fma_f32 v59, -v59, v68, v65
	v_div_fmas_f32 v59, v59, v64, v68
	v_div_fixup_f32 v49, v59, v49, v61
	v_div_scale_f32 v59, s[0:1], v48, v48, v60
	v_rcp_f32_e32 v61, v59
	s_nop 0
	v_fma_f32 v64, -v59, v61, 1.0
	v_fmac_f32_e32 v61, v64, v61
	v_div_scale_f32 v64, vcc, v60, v48, v60
	v_mul_f32_e32 v65, v64, v61
	v_fma_f32 v68, -v59, v65, v64
	v_fmac_f32_e32 v65, v68, v61
	v_fma_f32 v59, -v59, v65, v64
	v_div_fmas_f32 v59, v59, v61, v65
	v_div_fixup_f32 v48, v59, v48, v60
	v_mov_b64 v[60:61], v[218:219]
	v_lshlrev_b32_e32 v40, 16, v60
	v_mul_f32_e32 v38, 0xbfb8aa3b, v40
	v_fma_f32 v39, v40, s8, -v38
	v_rndne_f32_e32 v43, v38
	v_fmac_f32_e32 v39, 0xb2a5705f, v40
	v_sub_f32_e32 v38, v38, v43
	v_add_f32_e32 v38, v38, v39
	v_exp_f32_e32 v38, v38
	v_cvt_i32_f32_e32 v39, v43
	v_and_b32_e32 v41, 0xffff0000, v60
	v_cmp_nlt_f32_e32 vcc, s9, v40
	v_lshlrev_b32_e32 v65, 16, v61
	v_ldexp_f32 v38, v38, v39
	v_mul_f32_e32 v39, 0xbfb8aa3b, v41
	v_fma_f32 v43, v41, s8, -v39
	v_rndne_f32_e32 v44, v39
	v_fmac_f32_e32 v43, 0xb2a5705f, v41
	v_sub_f32_e32 v39, v39, v44
	v_add_f32_e32 v39, v39, v43
	v_exp_f32_e32 v39, v39
	v_cvt_i32_f32_e32 v43, v44
	v_cndmask_b32_e32 v38, 0, v38, vcc
	v_cmp_ngt_f32_e32 vcc, s10, v40
	v_and_b32_e32 v103, 0xffff0000, v61
	v_ldexp_f32 v39, v39, v43
	v_cndmask_b32_e32 v38, v191, v38, vcc
	v_cmp_nlt_f32_e32 vcc, s9, v41
	s_nop 1
	v_cndmask_b32_e32 v39, 0, v39, vcc
	v_cmp_ngt_f32_e32 vcc, s10, v41
	s_nop 1
	v_cndmask_b32_e32 v39, v191, v39, vcc
	v_pk_add_f32 v[38:39], v[38:39], 1.0 op_sel_hi:[1,0]
	s_nop 0
	v_div_scale_f32 v43, s[0:1], v39, v39, v41
	v_rcp_f32_e32 v44, v43
	s_nop 0
	v_fma_f32 v45, -v43, v44, 1.0
	v_fmac_f32_e32 v44, v45, v44
	v_div_scale_f32 v45, vcc, v41, v39, v41
	v_mul_f32_e32 v58, v45, v44
	v_fma_f32 v59, -v43, v58, v45
	v_fmac_f32_e32 v58, v59, v44
	v_fma_f32 v43, -v43, v58, v45
	v_div_fmas_f32 v43, v43, v44, v58
	v_div_fixup_f32 v41, v43, v39, v41
	v_div_scale_f32 v39, s[0:1], v38, v38, v40
	v_rcp_f32_e32 v43, v39
	s_nop 0
	v_fma_f32 v44, -v39, v43, 1.0
	v_fmac_f32_e32 v43, v44, v43
	v_div_scale_f32 v44, vcc, v40, v38, v40
	v_mul_f32_e32 v45, v44, v43
	v_fma_f32 v58, -v39, v45, v44
	v_fmac_f32_e32 v45, v58, v43
	v_fma_f32 v39, -v39, v45, v44
	v_div_fmas_f32 v39, v39, v43, v45
	v_div_fixup_f32 v40, v39, v38, v40
	v_add_f32_e32 v38, v36, v42
	v_add_f32_e32 v38, v37, v38
	v_add_f32_e32 v38, v38, v66
	v_add_f32_e32 v38, v67, v38
	v_add_f32_e32 v38, v56, v38
	v_add_f32_e32 v38, v57, v38
	v_add_f32_e32 v38, v38, v32
	v_add_f32_e32 v38, v33, v38
	v_add_f32_e32 v38, v108, v38
	v_add_f32_e32 v38, v109, v38
	ds_bpermute_b32 v39, v116, v38
	v_cmp_nlt_f32_e32 vcc, s9, v65
	s_waitcnt lgkmcnt(0)
	v_add_f32_e32 v38, v38, v39
	ds_bpermute_b32 v39, v117, v38
	s_waitcnt lgkmcnt(0)
	v_add_f32_e32 v38, v38, v39
	v_mul_f32_e32 v64, 0x3c800000, v38
	v_pk_add_f32 v[38:39], v[56:57], v[64:65] op_sel_hi:[1,0] neg_lo:[0,1] neg_hi:[0,1]
	v_mul_f32_e32 v56, 0xbfb8aa3b, v65
	v_fma_f32 v57, v65, s8, -v56
	v_rndne_f32_e32 v105, v56
	v_fmac_f32_e32 v57, 0xb2a5705f, v65
	v_sub_f32_e32 v56, v56, v105
	v_add_f32_e32 v56, v56, v57
	v_exp_f32_e32 v56, v56
	v_cvt_i32_f32_e32 v57, v105
	v_pk_add_f32 v[44:45], v[34:35], v[64:65] op_sel_hi:[1,0] neg_lo:[0,1] neg_hi:[0,1]
	v_pk_add_f32 v[34:35], v[32:33], v[64:65] op_sel_hi:[1,0] neg_lo:[0,1] neg_hi:[0,1]
	v_pk_add_f32 v[32:33], v[108:109], v[64:65] op_sel_hi:[1,0] neg_lo:[0,1] neg_hi:[0,1]
	v_ldexp_f32 v56, v56, v57
	v_mul_f32_e32 v57, 0xbfb8aa3b, v103
	v_fma_f32 v105, v103, s8, -v57
	v_rndne_f32_e32 v107, v57
	v_fmac_f32_e32 v105, 0xb2a5705f, v103
	v_sub_f32_e32 v57, v57, v107
	v_add_f32_e32 v57, v57, v105
	v_exp_f32_e32 v57, v57
	v_cvt_i32_f32_e32 v105, v107
	v_cndmask_b32_e32 v56, 0, v56, vcc
	v_cmp_ngt_f32_e32 vcc, s10, v65
	v_pk_add_f32 v[54:55], v[54:55], v[64:65] op_sel_hi:[1,0] neg_lo:[0,1] neg_hi:[0,1]
	v_ldexp_f32 v57, v57, v105
	v_cndmask_b32_e32 v56, v191, v56, vcc
	v_cmp_nlt_f32_e32 vcc, s9, v103
	v_pk_mul_f32 v[68:69], v[54:55], v[54:55]
	v_pk_add_f32 v[52:53], v[52:53], v[64:65] op_sel_hi:[1,0] neg_lo:[0,1] neg_hi:[0,1]
	v_cndmask_b32_e32 v57, 0, v57, vcc
	v_cmp_ngt_f32_e32 vcc, s10, v103
	v_pk_mul_f32 v[110:111], v[52:53], v[52:53]
	v_add_f32_e32 v68, v68, v69
	v_cndmask_b32_e32 v57, v191, v57, vcc
	v_pk_add_f32 v[56:57], v[56:57], 1.0 op_sel_hi:[1,0]
	v_add_f32_e32 v68, v110, v68
	v_div_scale_f32 v105, s[0:1], v57, v57, v103
	v_rcp_f32_e32 v107, v105
	v_pk_mul_f32 v[112:113], v[44:45], v[44:45]
	v_add_f32_e32 v68, v111, v68
	v_pk_add_f32 v[42:43], v[36:37], v[64:65] op_sel_hi:[1,0] neg_lo:[0,1] neg_hi:[0,1]
	v_fma_f32 v108, -v105, v107, 1.0
	v_fmac_f32_e32 v107, v108, v107
	v_div_scale_f32 v108, vcc, v103, v57, v103
	v_mul_f32_e32 v109, v108, v107
	v_fma_f32 v192, -v105, v109, v108
	v_fmac_f32_e32 v109, v192, v107
	v_fma_f32 v105, -v105, v109, v108
	v_div_fmas_f32 v105, v105, v107, v109
	v_div_fixup_f32 v57, v105, v57, v103
	v_div_scale_f32 v103, s[0:1], v56, v56, v65
	v_rcp_f32_e32 v105, v103
	v_add_f32_e32 v68, v112, v68
	v_pk_mul_f32 v[114:115], v[42:43], v[42:43]
	v_add_f32_e32 v68, v113, v68
	v_fma_f32 v107, -v103, v105, 1.0
	v_fmac_f32_e32 v105, v107, v105
	v_div_scale_f32 v107, vcc, v65, v56, v65
	v_mul_f32_e32 v108, v107, v105
	v_fma_f32 v109, -v103, v108, v107
	v_fmac_f32_e32 v108, v109, v105
	v_fma_f32 v103, -v103, v108, v107
	v_div_fmas_f32 v103, v103, v105, v108
	v_div_fixup_f32 v56, v103, v56, v65
	v_pk_add_f32 v[64:65], v[66:67], v[64:65] op_sel_hi:[1,0] neg_lo:[0,1] neg_hi:[0,1]
	v_add_f32_e32 v68, v114, v68
	v_pk_mul_f32 v[66:67], v[64:65], v[64:65]
	v_add_f32_e32 v68, v115, v68
	v_add_f32_e32 v66, v66, v68
	v_pk_mul_f32 v[36:37], v[38:39], v[38:39]
	v_add_f32_e32 v66, v67, v66
	v_add_f32_e32 v36, v36, v66
	v_pk_mul_f32 v[58:59], v[34:35], v[34:35]
	v_add_f32_e32 v36, v37, v36
	v_add_f32_e32 v36, v58, v36
	v_pk_mul_f32 v[60:61], v[32:33], v[32:33]
	v_add_f32_e32 v36, v59, v36
	v_add_f32_e32 v36, v60, v36
	v_add_f32_e32 v36, v61, v36
	ds_bpermute_b32 v37, v116, v36
	s_mov_b32 s0, 0xf800000
	v_mov_b64 v[108:109], v[220:221]
	s_waitcnt lgkmcnt(0)
	v_add_f32_e32 v36, v36, v37
	ds_bpermute_b32 v37, v117, v36
	s_waitcnt lgkmcnt(0)
	v_add_f32_e32 v36, v36, v37
	v_fmamk_f32 v36, v36, 0x3c800000, v189
	v_cmp_gt_f32_e32 vcc, s0, v36
	v_mul_f32_e32 v37, 0x4f800000, v36
	s_nop 0
	v_cndmask_b32_e32 v36, v36, v37, vcc
	v_sqrt_f32_e32 v37, v36
	s_nop 0
	v_add_u32_e32 v58, -1, v37
	v_fma_f32 v59, -v58, v37, v36
	v_cmp_ge_f32_e64 s[0:1], 0, v59
	v_add_u32_e32 v59, 1, v37
	s_nop 0
	v_cndmask_b32_e64 v58, v37, v58, s[0:1]
	v_fma_f32 v37, -v59, v37, v36
	v_cmp_lt_f32_e64 s[0:1], 0, v37
	s_nop 1
	v_cndmask_b32_e64 v37, v58, v59, s[0:1]
	v_mul_f32_e32 v58, 0x37800000, v37
	v_cndmask_b32_e32 v37, v37, v58, vcc
	v_cmp_class_f32_e32 vcc, v36, v190
	s_nop 1
	v_cndmask_b32_e32 v36, v37, v36, vcc
	v_div_scale_f32 v37, s[0:1], v36, v36, 1.0
	v_rcp_f32_e32 v58, v37
	s_nop 0
	v_fma_f32 v59, -v37, v58, 1.0
	v_fmac_f32_e32 v58, v59, v58
	v_div_scale_f32 v59, vcc, 1.0, v36, 1.0
	v_mul_f32_e32 v60, v59, v58
	v_fma_f32 v61, -v37, v60, v59
	v_fmac_f32_e32 v60, v61, v58
	v_fma_f32 v37, -v37, v60, v59
	v_div_fmas_f32 v37, v37, v58, v60
	v_div_fixup_f32 v36, v37, v36, 1.0
	v_pk_mul_f32 v[54:55], v[54:55], v[36:37] op_sel_hi:[1,0]
	v_pk_mul_f32 v[44:45], v[44:45], v[36:37] op_sel_hi:[1,0]
	v_pk_mul_f32 v[26:27], v[26:27], v[54:55]
	s_nop 0
	v_pk_mul_f32 v[26:27], v[50:51], v[26:27]
	v_pk_mul_f32 v[50:51], v[52:53], v[36:37] op_sel_hi:[1,0]
	v_cvt_pk_bf16_f32 v26, v26, v27
	v_pk_mul_f32 v[28:29], v[28:29], v[50:51]
	s_nop 0
	v_pk_mul_f32 v[28:29], v[48:49], v[28:29]
	s_nop 0
	v_cvt_pk_bf16_f32 v27, v28, v29
	global_store_dwordx2 v[30:31], v[26:27], off
	s_nop 1
	v_mov_b64 v[26:27], v[204:205]
	v_mov_b64 v[28:29], v[206:207]
	v_pk_mul_f32 v[26:27], v[26:27], v[44:45]
	s_nop 0
	v_pk_mul_f32 v[26:27], v[40:41], v[26:27]
	v_pk_mul_f32 v[40:41], v[42:43], v[36:37] op_sel_hi:[1,0]
	v_cvt_pk_bf16_f32 v26, v26, v27
	v_pk_mul_f32 v[28:29], v[28:29], v[40:41]
	v_lshlrev_b32_e32 v37, 16, v108
	v_pk_mul_f32 v[28:29], v[56:57], v[28:29]
	v_mul_f32_e32 v40, 0xbfb8aa3b, v37
	v_cvt_pk_bf16_f32 v27, v28, v29
	global_store_dwordx2 v[30:31], v[26:27], off offset:32
	s_nop 1
	v_mov_b64 v[26:27], v[208:209]
	v_mov_b64 v[28:29], v[210:211]
	v_fma_f32 v41, v37, s8, -v40
	v_rndne_f32_e32 v43, v40
	v_fmac_f32_e32 v41, 0xb2a5705f, v37
	v_sub_f32_e32 v40, v40, v43
	v_add_f32_e32 v40, v40, v41
	v_exp_f32_e32 v40, v40
	v_cvt_i32_f32_e32 v41, v43
	v_and_b32_e32 v42, 0xffff0000, v108
	v_cmp_nlt_f32_e32 vcc, s9, v37
	v_ldexp_f32 v40, v40, v41
	v_mul_f32_e32 v41, 0xbfb8aa3b, v42
	v_fma_f32 v43, v42, s8, -v41
	v_rndne_f32_e32 v44, v41
	v_fmac_f32_e32 v43, 0xb2a5705f, v42
	v_sub_f32_e32 v41, v41, v44
	v_add_f32_e32 v41, v41, v43
	v_exp_f32_e32 v41, v41
	v_cvt_i32_f32_e32 v43, v44
	v_cndmask_b32_e32 v40, 0, v40, vcc
	v_cmp_ngt_f32_e32 vcc, s10, v37
	v_ldexp_f32 v41, v41, v43
	s_nop 0
	v_cndmask_b32_e32 v40, v191, v40, vcc
	v_cmp_nlt_f32_e32 vcc, s9, v42
	s_nop 1
	v_cndmask_b32_e32 v41, 0, v41, vcc
	v_cmp_ngt_f32_e32 vcc, s10, v42
	s_nop 1
	v_cndmask_b32_e32 v41, v191, v41, vcc
	v_pk_add_f32 v[40:41], v[40:41], 1.0 op_sel_hi:[1,0]
	s_nop 0
	v_div_scale_f32 v43, s[0:1], v41, v41, v42
	v_rcp_f32_e32 v44, v43
	s_nop 0
	v_fma_f32 v45, -v43, v44, 1.0
	v_fmac_f32_e32 v44, v45, v44
	v_div_scale_f32 v45, vcc, v42, v41, v42
	v_mul_f32_e32 v48, v45, v44
	v_fma_f32 v49, -v43, v48, v45
	v_fmac_f32_e32 v48, v49, v44
	v_fma_f32 v43, -v43, v48, v45
	v_div_fmas_f32 v43, v43, v44, v48
	v_div_fixup_f32 v41, v43, v41, v42
	v_div_scale_f32 v42, s[0:1], v40, v40, v37
	v_rcp_f32_e32 v43, v42
	s_nop 0
	v_fma_f32 v44, -v42, v43, 1.0
	v_fmac_f32_e32 v43, v44, v43
	v_div_scale_f32 v44, vcc, v37, v40, v37
	v_mul_f32_e32 v45, v44, v43
	v_fma_f32 v48, -v42, v45, v44
	v_fmac_f32_e32 v45, v48, v43
	v_fma_f32 v42, -v42, v45, v44
	v_div_fmas_f32 v42, v42, v43, v45
	v_div_fixup_f32 v40, v42, v40, v37
	v_pk_mul_f32 v[42:43], v[64:65], v[36:37] op_sel_hi:[1,0]
	v_lshlrev_b32_e32 v37, 16, v109
	v_cmp_nlt_f32_e32 vcc, s9, v37
	v_pk_mul_f32 v[38:39], v[38:39], v[36:37] op_sel_hi:[1,0]
	v_pk_mul_f32 v[26:27], v[26:27], v[42:43]
	s_nop 0
	v_pk_mul_f32 v[26:27], v[40:41], v[26:27]
	v_mul_f32_e32 v40, 0xbfb8aa3b, v37
	v_fma_f32 v41, v37, s8, -v40
	v_rndne_f32_e32 v43, v40
	v_fmac_f32_e32 v41, 0xb2a5705f, v37
	v_sub_f32_e32 v40, v40, v43
	v_add_f32_e32 v40, v40, v41
	v_exp_f32_e32 v40, v40
	v_cvt_i32_f32_e32 v41, v43
	v_and_b32_e32 v42, 0xffff0000, v109
	v_pk_mul_f32 v[28:29], v[28:29], v[38:39]
	v_cvt_pk_bf16_f32 v26, v26, v27
	v_ldexp_f32 v40, v40, v41
	v_mul_f32_e32 v41, 0xbfb8aa3b, v42
	v_fma_f32 v43, v42, s8, -v41
	v_rndne_f32_e32 v44, v41
	v_fmac_f32_e32 v43, 0xb2a5705f, v42
	v_sub_f32_e32 v41, v41, v44
	v_add_f32_e32 v41, v41, v43
	v_exp_f32_e32 v41, v41
	v_cvt_i32_f32_e32 v43, v44
	v_cndmask_b32_e32 v40, 0, v40, vcc
	v_cmp_ngt_f32_e32 vcc, s10, v37
	v_ldexp_f32 v41, v41, v43
	s_nop 0
	v_cndmask_b32_e32 v40, v191, v40, vcc
	v_cmp_nlt_f32_e32 vcc, s9, v42
	s_nop 1
	v_cndmask_b32_e32 v41, 0, v41, vcc
	v_cmp_ngt_f32_e32 vcc, s10, v42
	s_nop 1
	v_cndmask_b32_e32 v41, v191, v41, vcc
	v_pk_add_f32 v[40:41], v[40:41], 1.0 op_sel_hi:[1,0]
	s_nop 0
	v_div_scale_f32 v43, s[0:1], v41, v41, v42
	v_rcp_f32_e32 v44, v43
	s_nop 0
	v_fma_f32 v45, -v43, v44, 1.0
	v_fmac_f32_e32 v44, v45, v44
	v_div_scale_f32 v45, vcc, v42, v41, v42
	v_mul_f32_e32 v48, v45, v44
	v_fma_f32 v49, -v43, v48, v45
	v_fmac_f32_e32 v48, v49, v44
	v_fma_f32 v43, -v43, v48, v45
	v_div_fmas_f32 v43, v43, v44, v48
	v_div_fixup_f32 v41, v43, v41, v42
	v_div_scale_f32 v42, s[0:1], v40, v40, v37
	v_rcp_f32_e32 v43, v42
	s_nop 0
	v_fma_f32 v44, -v42, v43, 1.0
	v_fmac_f32_e32 v43, v44, v43
	v_div_scale_f32 v44, vcc, v37, v40, v37
	v_mul_f32_e32 v45, v44, v43
	v_fma_f32 v48, -v42, v45, v44
	v_fmac_f32_e32 v45, v48, v43
	v_fma_f32 v42, -v42, v45, v44
	v_div_fmas_f32 v42, v42, v43, v45
	v_div_fixup_f32 v40, v42, v40, v37
	v_pk_mul_f32 v[28:29], v[40:41], v[28:29]
	s_nop 0
	v_cvt_pk_bf16_f32 v27, v28, v29
	global_store_dwordx2 v[30:31], v[26:27], off offset:64
	v_mov_b64 v[38:39], v[230:231]
	s_nop 0
	s_nop 1
	v_mov_b64 v[26:27], v[212:213]
	v_mov_b64 v[28:29], v[214:215]
	v_lshlrev_b32_e32 v37, 16, v38
	v_mul_f32_e32 v40, 0xbfb8aa3b, v37
	v_fma_f32 v41, v37, s8, -v40
	v_rndne_f32_e32 v42, v40
	v_fmac_f32_e32 v41, 0xb2a5705f, v37
	v_sub_f32_e32 v40, v40, v42
	v_add_f32_e32 v40, v40, v41
	v_exp_f32_e32 v40, v40
	v_cvt_i32_f32_e32 v41, v42
	v_and_b32_e32 v38, 0xffff0000, v38
	v_cmp_nlt_f32_e32 vcc, s9, v37
	v_pk_mul_f32 v[34:35], v[34:35], v[36:37] op_sel_hi:[1,0]
	v_ldexp_f32 v40, v40, v41
	v_mul_f32_e32 v41, 0xbfb8aa3b, v38
	v_fma_f32 v42, v38, s8, -v41
	v_rndne_f32_e32 v43, v41
	v_fmac_f32_e32 v42, 0xb2a5705f, v38
	v_sub_f32_e32 v41, v41, v43
	v_add_f32_e32 v41, v41, v42
	v_exp_f32_e32 v41, v41
	v_cvt_i32_f32_e32 v42, v43
	v_cndmask_b32_e32 v40, 0, v40, vcc
	v_cmp_ngt_f32_e32 vcc, s10, v37
	v_pk_mul_f32 v[26:27], v[26:27], v[34:35]
	v_ldexp_f32 v41, v41, v42
	v_cndmask_b32_e32 v40, v191, v40, vcc
	v_cmp_nlt_f32_e32 vcc, s9, v38
	s_nop 1
	v_cndmask_b32_e32 v41, 0, v41, vcc
	v_cmp_ngt_f32_e32 vcc, s10, v38
	s_nop 1
	v_cndmask_b32_e32 v41, v191, v41, vcc
	v_pk_add_f32 v[40:41], v[40:41], 1.0 op_sel_hi:[1,0]
	s_nop 0
	v_div_scale_f32 v42, s[0:1], v41, v41, v38
	v_rcp_f32_e32 v43, v42
	s_nop 0
	v_fma_f32 v44, -v42, v43, 1.0
	v_fmac_f32_e32 v43, v44, v43
	v_div_scale_f32 v44, vcc, v38, v41, v38
	v_mul_f32_e32 v45, v44, v43
	v_fma_f32 v46, -v42, v45, v44
	v_fmac_f32_e32 v45, v46, v43
	v_fma_f32 v42, -v42, v45, v44
	v_div_fmas_f32 v42, v42, v43, v45
	v_div_fixup_f32 v41, v42, v41, v38
	v_div_scale_f32 v38, s[0:1], v40, v40, v37
	v_rcp_f32_e32 v42, v38
	s_nop 0
	v_fma_f32 v43, -v38, v42, 1.0
	v_fmac_f32_e32 v42, v43, v42
	v_div_scale_f32 v43, vcc, v37, v40, v37
	v_mul_f32_e32 v44, v43, v42
	v_fma_f32 v45, -v38, v44, v43
	v_fmac_f32_e32 v44, v45, v42
	v_fma_f32 v38, -v38, v44, v43
	v_div_fmas_f32 v38, v38, v42, v44
	v_div_fixup_f32 v40, v38, v40, v37
	v_lshlrev_b32_e32 v37, 16, v39
	v_mul_f32_e32 v34, 0xbfb8aa3b, v37
	v_and_b32_e32 v38, 0xffff0000, v39
	v_fma_f32 v35, v37, s8, -v34
	v_rndne_f32_e32 v39, v34
	v_fmac_f32_e32 v35, 0xb2a5705f, v37
	v_sub_f32_e32 v34, v34, v39
	v_add_f32_e32 v34, v34, v35
	v_exp_f32_e32 v34, v34
	v_cvt_i32_f32_e32 v35, v39
	v_pk_mul_f32 v[26:27], v[40:41], v[26:27]
	v_cmp_nlt_f32_e32 vcc, s9, v37
	v_pk_mul_f32 v[32:33], v[32:33], v[36:37] op_sel_hi:[1,0]
	v_ldexp_f32 v34, v34, v35
	v_mul_f32_e32 v35, 0xbfb8aa3b, v38
	v_fma_f32 v39, v38, s8, -v35
	v_rndne_f32_e32 v40, v35
	v_fmac_f32_e32 v39, 0xb2a5705f, v38
	v_sub_f32_e32 v35, v35, v40
	v_add_f32_e32 v35, v35, v39
	v_exp_f32_e32 v35, v35
	v_cvt_i32_f32_e32 v39, v40
	v_cndmask_b32_e32 v34, 0, v34, vcc
	v_cmp_ngt_f32_e32 vcc, s10, v37
	v_pk_mul_f32 v[28:29], v[28:29], v[32:33]
	v_ldexp_f32 v35, v35, v39
	v_cndmask_b32_e32 v34, v191, v34, vcc
	v_cmp_nlt_f32_e32 vcc, s9, v38
	v_cvt_pk_bf16_f32 v26, v26, v27
	s_nop 0
	v_cndmask_b32_e32 v35, 0, v35, vcc
	v_cmp_ngt_f32_e32 vcc, s10, v38
	s_nop 1
	v_cndmask_b32_e32 v35, v191, v35, vcc
	v_pk_add_f32 v[34:35], v[34:35], 1.0 op_sel_hi:[1,0]
	s_nop 0
	v_div_scale_f32 v39, s[0:1], v35, v35, v38
	v_rcp_f32_e32 v40, v39
	s_nop 0
	v_fma_f32 v41, -v39, v40, 1.0
	v_fmac_f32_e32 v40, v41, v40
	v_div_scale_f32 v41, vcc, v38, v35, v38
	v_mul_f32_e32 v42, v41, v40
	v_fma_f32 v43, -v39, v42, v41
	v_fmac_f32_e32 v42, v43, v40
	v_fma_f32 v39, -v39, v42, v41
	v_div_fmas_f32 v39, v39, v40, v42
	v_div_fixup_f32 v35, v39, v35, v38
	v_div_scale_f32 v38, s[0:1], v34, v34, v37
	v_rcp_f32_e32 v39, v38
	s_nop 0
	v_fma_f32 v40, -v38, v39, 1.0
	v_fmac_f32_e32 v39, v40, v39
	v_div_scale_f32 v40, vcc, v37, v34, v37
	v_mul_f32_e32 v41, v40, v39
	v_fma_f32 v42, -v38, v41, v40
	v_fmac_f32_e32 v41, v42, v39
	v_fma_f32 v38, -v38, v41, v40
	v_div_fmas_f32 v38, v38, v39, v41
	v_div_fixup_f32 v34, v38, v34, v37
	v_pk_mul_f32 v[28:29], v[34:35], v[28:29]
	s_andn2_b64 vcc, exec, s[88:89]
	v_cvt_pk_bf16_f32 v27, v28, v29
	global_store_dwordx2 v[30:31], v[26:27], off offset:96
	s_cbranch_vccz .LBB0_3604
